# GLA decay cumulative sums (phase 1 chunk states, phase 3 GLA output): 192 serialized ds_bpermute shuffles per wave job replaced by an in-register DPP scan (row_shr 1,2,4,8 + row_bcast 15,31), f32
# speedup vs baseline: 1.0158x; 1.0114x over previous
.LBB0_361:
	s_ashr_i32 s14, s18, 2
	s_ashr_i32 s15, s14, 31
	s_lshl_b64 s[30:31], s[14:15], 15
	v_mov_b32_e32 v13, s31
	v_or_b32_e32 v12, s30, v34
	v_lshl_add_u64 v[30:31], s[26:27], 0, v[12:13]
	global_load_dwordx4 v[14:17], v[30:31], off
	global_load_dwordx4 v[18:21], v[30:31], off offset:16
	global_load_dwordx4 v[22:25], v[30:31], off offset:32
	global_load_dwordx4 v[26:29], v[30:31], off offset:48
	s_waitcnt lgkmcnt(0)
	global_load_dwordx4 v[0:3], v[30:31], off offset:112
	global_load_dwordx4 v[4:7], v[30:31], off offset:96
	global_load_dwordx4 v[8:11], v[30:31], off offset:80
	global_load_dwordx4 v[76:79], v[30:31], off offset:64
	s_waitcnt vmcnt(0)
	s_nop 1
	v_add_f32_dpp v14, v14, v14 row_shr:1 row_mask:0xf bank_mask:0xf bound_ctrl:0
	v_add_f32_dpp v15, v15, v15 row_shr:1 row_mask:0xf bank_mask:0xf bound_ctrl:0
	v_add_f32_dpp v16, v16, v16 row_shr:1 row_mask:0xf bank_mask:0xf bound_ctrl:0
	v_add_f32_dpp v17, v17, v17 row_shr:1 row_mask:0xf bank_mask:0xf bound_ctrl:0
	v_add_f32_dpp v18, v18, v18 row_shr:1 row_mask:0xf bank_mask:0xf bound_ctrl:0
	v_add_f32_dpp v19, v19, v19 row_shr:1 row_mask:0xf bank_mask:0xf bound_ctrl:0
	v_add_f32_dpp v20, v20, v20 row_shr:1 row_mask:0xf bank_mask:0xf bound_ctrl:0
	v_add_f32_dpp v21, v21, v21 row_shr:1 row_mask:0xf bank_mask:0xf bound_ctrl:0
	v_add_f32_dpp v14, v14, v14 row_shr:2 row_mask:0xf bank_mask:0xf bound_ctrl:0
	v_add_f32_dpp v15, v15, v15 row_shr:2 row_mask:0xf bank_mask:0xf bound_ctrl:0
	v_add_f32_dpp v16, v16, v16 row_shr:2 row_mask:0xf bank_mask:0xf bound_ctrl:0
	v_add_f32_dpp v17, v17, v17 row_shr:2 row_mask:0xf bank_mask:0xf bound_ctrl:0
	v_add_f32_dpp v18, v18, v18 row_shr:2 row_mask:0xf bank_mask:0xf bound_ctrl:0
	v_add_f32_dpp v19, v19, v19 row_shr:2 row_mask:0xf bank_mask:0xf bound_ctrl:0
	v_add_f32_dpp v20, v20, v20 row_shr:2 row_mask:0xf bank_mask:0xf bound_ctrl:0
	v_add_f32_dpp v21, v21, v21 row_shr:2 row_mask:0xf bank_mask:0xf bound_ctrl:0
	v_add_f32_dpp v14, v14, v14 row_shr:4 row_mask:0xf bank_mask:0xf bound_ctrl:0
	v_add_f32_dpp v15, v15, v15 row_shr:4 row_mask:0xf bank_mask:0xf bound_ctrl:0
	v_add_f32_dpp v16, v16, v16 row_shr:4 row_mask:0xf bank_mask:0xf bound_ctrl:0
	v_add_f32_dpp v17, v17, v17 row_shr:4 row_mask:0xf bank_mask:0xf bound_ctrl:0
	v_add_f32_dpp v18, v18, v18 row_shr:4 row_mask:0xf bank_mask:0xf bound_ctrl:0
	v_add_f32_dpp v19, v19, v19 row_shr:4 row_mask:0xf bank_mask:0xf bound_ctrl:0
	v_add_f32_dpp v20, v20, v20 row_shr:4 row_mask:0xf bank_mask:0xf bound_ctrl:0
	v_add_f32_dpp v21, v21, v21 row_shr:4 row_mask:0xf bank_mask:0xf bound_ctrl:0
	v_add_f32_dpp v14, v14, v14 row_shr:8 row_mask:0xf bank_mask:0xf bound_ctrl:0
	v_add_f32_dpp v15, v15, v15 row_shr:8 row_mask:0xf bank_mask:0xf bound_ctrl:0
	v_add_f32_dpp v16, v16, v16 row_shr:8 row_mask:0xf bank_mask:0xf bound_ctrl:0
	v_add_f32_dpp v17, v17, v17 row_shr:8 row_mask:0xf bank_mask:0xf bound_ctrl:0
	v_add_f32_dpp v18, v18, v18 row_shr:8 row_mask:0xf bank_mask:0xf bound_ctrl:0
	v_add_f32_dpp v19, v19, v19 row_shr:8 row_mask:0xf bank_mask:0xf bound_ctrl:0
	v_add_f32_dpp v20, v20, v20 row_shr:8 row_mask:0xf bank_mask:0xf bound_ctrl:0
	v_add_f32_dpp v21, v21, v21 row_shr:8 row_mask:0xf bank_mask:0xf bound_ctrl:0
	v_add_f32_dpp v14, v14, v14 row_bcast:15 row_mask:0xa bank_mask:0xf
	v_add_f32_dpp v15, v15, v15 row_bcast:15 row_mask:0xa bank_mask:0xf
	v_add_f32_dpp v16, v16, v16 row_bcast:15 row_mask:0xa bank_mask:0xf
	v_add_f32_dpp v17, v17, v17 row_bcast:15 row_mask:0xa bank_mask:0xf
	v_add_f32_dpp v18, v18, v18 row_bcast:15 row_mask:0xa bank_mask:0xf
	v_add_f32_dpp v19, v19, v19 row_bcast:15 row_mask:0xa bank_mask:0xf
	v_add_f32_dpp v20, v20, v20 row_bcast:15 row_mask:0xa bank_mask:0xf
	v_add_f32_dpp v21, v21, v21 row_bcast:15 row_mask:0xa bank_mask:0xf
	v_add_f32_dpp v14, v14, v14 row_bcast:31 row_mask:0xc bank_mask:0xf
	v_add_f32_dpp v15, v15, v15 row_bcast:31 row_mask:0xc bank_mask:0xf
	v_add_f32_dpp v16, v16, v16 row_bcast:31 row_mask:0xc bank_mask:0xf
	v_add_f32_dpp v17, v17, v17 row_bcast:31 row_mask:0xc bank_mask:0xf
	v_add_f32_dpp v18, v18, v18 row_bcast:31 row_mask:0xc bank_mask:0xf
	v_add_f32_dpp v19, v19, v19 row_bcast:31 row_mask:0xc bank_mask:0xf
	v_add_f32_dpp v20, v20, v20 row_bcast:31 row_mask:0xc bank_mask:0xf
	v_add_f32_dpp v21, v21, v21 row_bcast:31 row_mask:0xc bank_mask:0xf
	v_add_f32_dpp v22, v22, v22 row_shr:1 row_mask:0xf bank_mask:0xf bound_ctrl:0
	v_add_f32_dpp v23, v23, v23 row_shr:1 row_mask:0xf bank_mask:0xf bound_ctrl:0
	v_add_f32_dpp v24, v24, v24 row_shr:1 row_mask:0xf bank_mask:0xf bound_ctrl:0
	v_add_f32_dpp v25, v25, v25 row_shr:1 row_mask:0xf bank_mask:0xf bound_ctrl:0
	v_add_f32_dpp v26, v26, v26 row_shr:1 row_mask:0xf bank_mask:0xf bound_ctrl:0
	v_add_f32_dpp v27, v27, v27 row_shr:1 row_mask:0xf bank_mask:0xf bound_ctrl:0
	v_add_f32_dpp v28, v28, v28 row_shr:1 row_mask:0xf bank_mask:0xf bound_ctrl:0
	v_add_f32_dpp v29, v29, v29 row_shr:1 row_mask:0xf bank_mask:0xf bound_ctrl:0
	v_add_f32_dpp v22, v22, v22 row_shr:2 row_mask:0xf bank_mask:0xf bound_ctrl:0
	v_add_f32_dpp v23, v23, v23 row_shr:2 row_mask:0xf bank_mask:0xf bound_ctrl:0
	v_add_f32_dpp v24, v24, v24 row_shr:2 row_mask:0xf bank_mask:0xf bound_ctrl:0
	v_add_f32_dpp v25, v25, v25 row_shr:2 row_mask:0xf bank_mask:0xf bound_ctrl:0
	v_add_f32_dpp v26, v26, v26 row_shr:2 row_mask:0xf bank_mask:0xf bound_ctrl:0
	v_add_f32_dpp v27, v27, v27 row_shr:2 row_mask:0xf bank_mask:0xf bound_ctrl:0
	v_add_f32_dpp v28, v28, v28 row_shr:2 row_mask:0xf bank_mask:0xf bound_ctrl:0
	v_add_f32_dpp v29, v29, v29 row_shr:2 row_mask:0xf bank_mask:0xf bound_ctrl:0
	v_add_f32_dpp v22, v22, v22 row_shr:4 row_mask:0xf bank_mask:0xf bound_ctrl:0
	v_add_f32_dpp v23, v23, v23 row_shr:4 row_mask:0xf bank_mask:0xf bound_ctrl:0
	v_add_f32_dpp v24, v24, v24 row_shr:4 row_mask:0xf bank_mask:0xf bound_ctrl:0
	v_add_f32_dpp v25, v25, v25 row_shr:4 row_mask:0xf bank_mask:0xf bound_ctrl:0
	v_add_f32_dpp v26, v26, v26 row_shr:4 row_mask:0xf bank_mask:0xf bound_ctrl:0
	v_add_f32_dpp v27, v27, v27 row_shr:4 row_mask:0xf bank_mask:0xf bound_ctrl:0
	v_add_f32_dpp v28, v28, v28 row_shr:4 row_mask:0xf bank_mask:0xf bound_ctrl:0
	v_add_f32_dpp v29, v29, v29 row_shr:4 row_mask:0xf bank_mask:0xf bound_ctrl:0
	v_add_f32_dpp v22, v22, v22 row_shr:8 row_mask:0xf bank_mask:0xf bound_ctrl:0
	v_add_f32_dpp v23, v23, v23 row_shr:8 row_mask:0xf bank_mask:0xf bound_ctrl:0
	v_add_f32_dpp v24, v24, v24 row_shr:8 row_mask:0xf bank_mask:0xf bound_ctrl:0
	v_add_f32_dpp v25, v25, v25 row_shr:8 row_mask:0xf bank_mask:0xf bound_ctrl:0
	v_add_f32_dpp v26, v26, v26 row_shr:8 row_mask:0xf bank_mask:0xf bound_ctrl:0
	v_add_f32_dpp v27, v27, v27 row_shr:8 row_mask:0xf bank_mask:0xf bound_ctrl:0
	v_add_f32_dpp v28, v28, v28 row_shr:8 row_mask:0xf bank_mask:0xf bound_ctrl:0
	v_add_f32_dpp v29, v29, v29 row_shr:8 row_mask:0xf bank_mask:0xf bound_ctrl:0
	v_add_f32_dpp v22, v22, v22 row_bcast:15 row_mask:0xa bank_mask:0xf
	v_add_f32_dpp v23, v23, v23 row_bcast:15 row_mask:0xa bank_mask:0xf
	v_add_f32_dpp v24, v24, v24 row_bcast:15 row_mask:0xa bank_mask:0xf
	v_add_f32_dpp v25, v25, v25 row_bcast:15 row_mask:0xa bank_mask:0xf
	v_add_f32_dpp v26, v26, v26 row_bcast:15 row_mask:0xa bank_mask:0xf
	v_add_f32_dpp v27, v27, v27 row_bcast:15 row_mask:0xa bank_mask:0xf
	v_add_f32_dpp v28, v28, v28 row_bcast:15 row_mask:0xa bank_mask:0xf
	v_add_f32_dpp v29, v29, v29 row_bcast:15 row_mask:0xa bank_mask:0xf
	v_add_f32_dpp v22, v22, v22 row_bcast:31 row_mask:0xc bank_mask:0xf
	v_add_f32_dpp v23, v23, v23 row_bcast:31 row_mask:0xc bank_mask:0xf
	v_add_f32_dpp v24, v24, v24 row_bcast:31 row_mask:0xc bank_mask:0xf
	v_add_f32_dpp v25, v25, v25 row_bcast:31 row_mask:0xc bank_mask:0xf
	v_add_f32_dpp v26, v26, v26 row_bcast:31 row_mask:0xc bank_mask:0xf
	v_add_f32_dpp v27, v27, v27 row_bcast:31 row_mask:0xc bank_mask:0xf
	v_add_f32_dpp v28, v28, v28 row_bcast:31 row_mask:0xc bank_mask:0xf
	v_add_f32_dpp v29, v29, v29 row_bcast:31 row_mask:0xc bank_mask:0xf
	v_add_f32_dpp v76, v76, v76 row_shr:1 row_mask:0xf bank_mask:0xf bound_ctrl:0
	v_add_f32_dpp v77, v77, v77 row_shr:1 row_mask:0xf bank_mask:0xf bound_ctrl:0
	v_add_f32_dpp v78, v78, v78 row_shr:1 row_mask:0xf bank_mask:0xf bound_ctrl:0
	v_add_f32_dpp v79, v79, v79 row_shr:1 row_mask:0xf bank_mask:0xf bound_ctrl:0
	v_add_f32_dpp v8, v8, v8 row_shr:1 row_mask:0xf bank_mask:0xf bound_ctrl:0
	v_add_f32_dpp v9, v9, v9 row_shr:1 row_mask:0xf bank_mask:0xf bound_ctrl:0
	v_add_f32_dpp v10, v10, v10 row_shr:1 row_mask:0xf bank_mask:0xf bound_ctrl:0
	v_add_f32_dpp v11, v11, v11 row_shr:1 row_mask:0xf bank_mask:0xf bound_ctrl:0
	v_add_f32_dpp v76, v76, v76 row_shr:2 row_mask:0xf bank_mask:0xf bound_ctrl:0
	v_add_f32_dpp v77, v77, v77 row_shr:2 row_mask:0xf bank_mask:0xf bound_ctrl:0
	v_add_f32_dpp v78, v78, v78 row_shr:2 row_mask:0xf bank_mask:0xf bound_ctrl:0
	v_add_f32_dpp v79, v79, v79 row_shr:2 row_mask:0xf bank_mask:0xf bound_ctrl:0
	v_add_f32_dpp v8, v8, v8 row_shr:2 row_mask:0xf bank_mask:0xf bound_ctrl:0
	v_add_f32_dpp v9, v9, v9 row_shr:2 row_mask:0xf bank_mask:0xf bound_ctrl:0
	v_add_f32_dpp v10, v10, v10 row_shr:2 row_mask:0xf bank_mask:0xf bound_ctrl:0
	v_add_f32_dpp v11, v11, v11 row_shr:2 row_mask:0xf bank_mask:0xf bound_ctrl:0
	v_add_f32_dpp v76, v76, v76 row_shr:4 row_mask:0xf bank_mask:0xf bound_ctrl:0
	v_add_f32_dpp v77, v77, v77 row_shr:4 row_mask:0xf bank_mask:0xf bound_ctrl:0
	v_add_f32_dpp v78, v78, v78 row_shr:4 row_mask:0xf bank_mask:0xf bound_ctrl:0
	v_add_f32_dpp v79, v79, v79 row_shr:4 row_mask:0xf bank_mask:0xf bound_ctrl:0
	v_add_f32_dpp v8, v8, v8 row_shr:4 row_mask:0xf bank_mask:0xf bound_ctrl:0
	v_add_f32_dpp v9, v9, v9 row_shr:4 row_mask:0xf bank_mask:0xf bound_ctrl:0
	v_add_f32_dpp v10, v10, v10 row_shr:4 row_mask:0xf bank_mask:0xf bound_ctrl:0
	v_add_f32_dpp v11, v11, v11 row_shr:4 row_mask:0xf bank_mask:0xf bound_ctrl:0
	v_add_f32_dpp v76, v76, v76 row_shr:8 row_mask:0xf bank_mask:0xf bound_ctrl:0
	v_add_f32_dpp v77, v77, v77 row_shr:8 row_mask:0xf bank_mask:0xf bound_ctrl:0
	v_add_f32_dpp v78, v78, v78 row_shr:8 row_mask:0xf bank_mask:0xf bound_ctrl:0
	v_add_f32_dpp v79, v79, v79 row_shr:8 row_mask:0xf bank_mask:0xf bound_ctrl:0
	v_add_f32_dpp v8, v8, v8 row_shr:8 row_mask:0xf bank_mask:0xf bound_ctrl:0
	v_add_f32_dpp v9, v9, v9 row_shr:8 row_mask:0xf bank_mask:0xf bound_ctrl:0
	v_add_f32_dpp v10, v10, v10 row_shr:8 row_mask:0xf bank_mask:0xf bound_ctrl:0
	v_add_f32_dpp v11, v11, v11 row_shr:8 row_mask:0xf bank_mask:0xf bound_ctrl:0
	v_add_f32_dpp v76, v76, v76 row_bcast:15 row_mask:0xa bank_mask:0xf
	v_add_f32_dpp v77, v77, v77 row_bcast:15 row_mask:0xa bank_mask:0xf
	v_add_f32_dpp v78, v78, v78 row_bcast:15 row_mask:0xa bank_mask:0xf
	v_add_f32_dpp v79, v79, v79 row_bcast:15 row_mask:0xa bank_mask:0xf
	v_add_f32_dpp v8, v8, v8 row_bcast:15 row_mask:0xa bank_mask:0xf
	v_add_f32_dpp v9, v9, v9 row_bcast:15 row_mask:0xa bank_mask:0xf
	v_add_f32_dpp v10, v10, v10 row_bcast:15 row_mask:0xa bank_mask:0xf
	v_add_f32_dpp v11, v11, v11 row_bcast:15 row_mask:0xa bank_mask:0xf
	v_add_f32_dpp v76, v76, v76 row_bcast:31 row_mask:0xc bank_mask:0xf
	v_add_f32_dpp v77, v77, v77 row_bcast:31 row_mask:0xc bank_mask:0xf
	v_add_f32_dpp v78, v78, v78 row_bcast:31 row_mask:0xc bank_mask:0xf
	v_add_f32_dpp v79, v79, v79 row_bcast:31 row_mask:0xc bank_mask:0xf
	v_add_f32_dpp v8, v8, v8 row_bcast:31 row_mask:0xc bank_mask:0xf
	v_add_f32_dpp v9, v9, v9 row_bcast:31 row_mask:0xc bank_mask:0xf
	v_add_f32_dpp v10, v10, v10 row_bcast:31 row_mask:0xc bank_mask:0xf
	v_add_f32_dpp v11, v11, v11 row_bcast:31 row_mask:0xc bank_mask:0xf
	v_add_f32_dpp v4, v4, v4 row_shr:1 row_mask:0xf bank_mask:0xf bound_ctrl:0
	v_add_f32_dpp v5, v5, v5 row_shr:1 row_mask:0xf bank_mask:0xf bound_ctrl:0
	v_add_f32_dpp v6, v6, v6 row_shr:1 row_mask:0xf bank_mask:0xf bound_ctrl:0
	v_add_f32_dpp v7, v7, v7 row_shr:1 row_mask:0xf bank_mask:0xf bound_ctrl:0
	v_add_f32_dpp v0, v0, v0 row_shr:1 row_mask:0xf bank_mask:0xf bound_ctrl:0
	v_add_f32_dpp v1, v1, v1 row_shr:1 row_mask:0xf bank_mask:0xf bound_ctrl:0
	v_add_f32_dpp v2, v2, v2 row_shr:1 row_mask:0xf bank_mask:0xf bound_ctrl:0
	v_add_f32_dpp v3, v3, v3 row_shr:1 row_mask:0xf bank_mask:0xf bound_ctrl:0
	v_add_f32_dpp v4, v4, v4 row_shr:2 row_mask:0xf bank_mask:0xf bound_ctrl:0
	v_add_f32_dpp v5, v5, v5 row_shr:2 row_mask:0xf bank_mask:0xf bound_ctrl:0
	v_add_f32_dpp v6, v6, v6 row_shr:2 row_mask:0xf bank_mask:0xf bound_ctrl:0
	v_add_f32_dpp v7, v7, v7 row_shr:2 row_mask:0xf bank_mask:0xf bound_ctrl:0
	v_add_f32_dpp v0, v0, v0 row_shr:2 row_mask:0xf bank_mask:0xf bound_ctrl:0
	v_add_f32_dpp v1, v1, v1 row_shr:2 row_mask:0xf bank_mask:0xf bound_ctrl:0
	v_add_f32_dpp v2, v2, v2 row_shr:2 row_mask:0xf bank_mask:0xf bound_ctrl:0
	v_add_f32_dpp v3, v3, v3 row_shr:2 row_mask:0xf bank_mask:0xf bound_ctrl:0
	v_add_f32_dpp v4, v4, v4 row_shr:4 row_mask:0xf bank_mask:0xf bound_ctrl:0
	v_add_f32_dpp v5, v5, v5 row_shr:4 row_mask:0xf bank_mask:0xf bound_ctrl:0
	v_add_f32_dpp v6, v6, v6 row_shr:4 row_mask:0xf bank_mask:0xf bound_ctrl:0
	v_add_f32_dpp v7, v7, v7 row_shr:4 row_mask:0xf bank_mask:0xf bound_ctrl:0
	v_add_f32_dpp v0, v0, v0 row_shr:4 row_mask:0xf bank_mask:0xf bound_ctrl:0
	v_add_f32_dpp v1, v1, v1 row_shr:4 row_mask:0xf bank_mask:0xf bound_ctrl:0
	v_add_f32_dpp v2, v2, v2 row_shr:4 row_mask:0xf bank_mask:0xf bound_ctrl:0
	v_add_f32_dpp v3, v3, v3 row_shr:4 row_mask:0xf bank_mask:0xf bound_ctrl:0
	v_add_f32_dpp v4, v4, v4 row_shr:8 row_mask:0xf bank_mask:0xf bound_ctrl:0
	v_add_f32_dpp v5, v5, v5 row_shr:8 row_mask:0xf bank_mask:0xf bound_ctrl:0
	v_add_f32_dpp v6, v6, v6 row_shr:8 row_mask:0xf bank_mask:0xf bound_ctrl:0
	v_add_f32_dpp v7, v7, v7 row_shr:8 row_mask:0xf bank_mask:0xf bound_ctrl:0
	v_add_f32_dpp v0, v0, v0 row_shr:8 row_mask:0xf bank_mask:0xf bound_ctrl:0
	v_add_f32_dpp v1, v1, v1 row_shr:8 row_mask:0xf bank_mask:0xf bound_ctrl:0
	v_add_f32_dpp v2, v2, v2 row_shr:8 row_mask:0xf bank_mask:0xf bound_ctrl:0
	v_add_f32_dpp v3, v3, v3 row_shr:8 row_mask:0xf bank_mask:0xf bound_ctrl:0
	v_add_f32_dpp v4, v4, v4 row_bcast:15 row_mask:0xa bank_mask:0xf
	v_add_f32_dpp v5, v5, v5 row_bcast:15 row_mask:0xa bank_mask:0xf
	v_add_f32_dpp v6, v6, v6 row_bcast:15 row_mask:0xa bank_mask:0xf
	v_add_f32_dpp v7, v7, v7 row_bcast:15 row_mask:0xa bank_mask:0xf
	v_add_f32_dpp v0, v0, v0 row_bcast:15 row_mask:0xa bank_mask:0xf
	v_add_f32_dpp v1, v1, v1 row_bcast:15 row_mask:0xa bank_mask:0xf
	v_add_f32_dpp v2, v2, v2 row_bcast:15 row_mask:0xa bank_mask:0xf
	v_add_f32_dpp v3, v3, v3 row_bcast:15 row_mask:0xa bank_mask:0xf
	v_add_f32_dpp v4, v4, v4 row_bcast:31 row_mask:0xc bank_mask:0xf
	v_add_f32_dpp v5, v5, v5 row_bcast:31 row_mask:0xc bank_mask:0xf
	v_add_f32_dpp v6, v6, v6 row_bcast:31 row_mask:0xc bank_mask:0xf
	v_add_f32_dpp v7, v7, v7 row_bcast:31 row_mask:0xc bank_mask:0xf
	v_add_f32_dpp v0, v0, v0 row_bcast:31 row_mask:0xc bank_mask:0xf
	v_add_f32_dpp v1, v1, v1 row_bcast:31 row_mask:0xc bank_mask:0xf
	v_add_f32_dpp v2, v2, v2 row_bcast:31 row_mask:0xc bank_mask:0xf
	v_add_f32_dpp v3, v3, v3 row_bcast:31 row_mask:0xc bank_mask:0xf
	v_mov_b32_e32 v90, v14
	v_mov_b32_e32 v91, v15
	v_mov_b32_e32 v92, v16
	v_mov_b32_e32 v93, v17
	v_mov_b32_e32 v30, v76
	v_mov_b32_e32 v31, v77
	v_mov_b32_e32 v81, v10
	v_mov_b32_e32 v82, v11
	v_mov_b32_e32 v80, v4
	v_mov_b32_e32 v83, v5
	v_mov_b32_e32 v84, v6
	v_mov_b32_e32 v85, v7
	v_mov_b32_e32 v86, v0
	v_mov_b32_e32 v87, v1
	v_mov_b32_e32 v88, v2
	v_mov_b32_e32 v89, v3
	v_mov_b32_e32 v76, v78
	v_mov_b32_e32 v77, v79
	v_mov_b32_e32 v78, v8
	v_mov_b32_e32 v79, v9
	s_nop 0
	s_mov_b32 s15, 0x3ab00000
	s_mov_b64 s[30:31], 0x3ab00100
	s_waitcnt lgkmcnt(0)
	s_nop 0
	v_readlane_b32 s19, v91, 63
	s_nop 0
	v_sub_f32_e32 v91, s19, v91
	s_waitcnt lgkmcnt(0)
	s_waitcnt lgkmcnt(0)
	v_mul_f32_e32 v91, 0x3fb8aa3b, v91
	v_exp_f32_e32 v91, v91
	v_readlane_b32 s48, v93, 63
	s_waitcnt lgkmcnt(0)
	s_nop 0
	v_readlane_b32 s50, v18, 63
	s_nop 0
	s_waitcnt lgkmcnt(0)
	s_waitcnt lgkmcnt(0)
	s_waitcnt lgkmcnt(0)
	v_readlane_b32 s49, v20, 63
	v_readlane_b32 s51, v21, 63
	s_nop 0
	s_waitcnt lgkmcnt(0)
	s_waitcnt lgkmcnt(0)
	v_readlane_b32 s52, v22, 63
	v_readlane_b32 s53, v23, 63
	s_waitcnt lgkmcnt(0)
	s_nop 0
	v_readlane_b32 s54, v24, 63
	s_nop 0
	s_waitcnt lgkmcnt(0)
	s_waitcnt lgkmcnt(0)
	v_readlane_b32 s56, v25, 63
	v_readlane_b32 s55, v26, 63
	s_waitcnt lgkmcnt(0)
	s_nop 0
	v_readlane_b32 s57, v27, 63
	s_nop 0
	s_waitcnt lgkmcnt(0)
	s_waitcnt lgkmcnt(0)
	v_readlane_b32 s58, v28, 63
	v_readlane_b32 s59, v29, 63
	s_waitcnt lgkmcnt(0)
	s_nop 0
	v_readlane_b32 s60, v30, 63
	s_nop 0
	s_waitcnt lgkmcnt(0)
	s_waitcnt lgkmcnt(0)
	v_readlane_b32 s61, v31, 63
	v_readlane_b32 s62, v76, 63
	s_waitcnt lgkmcnt(0)
	s_nop 0
	v_readlane_b32 s63, v77, 63
	s_nop 0
	s_nop 0
	s_nop 1
	v_lshl_add_u64 v[0:1], s[20:21], 0, v[12:13]
	v_lshl_add_u64 v[4:5], v[0:1], 0, s[86:87]
	v_add_co_u32_e32 v0, vcc, s15, v4
	s_nop 0
	v_addc_co_u32_e32 v1, vcc, 0, v5, vcc
	global_load_dwordx4 v[0:3], v[0:1], off offset:256
	v_lshl_add_u64 v[14:15], v[4:5], 0, s[30:31]
	s_waitcnt lgkmcnt(1)
	global_load_dwordx4 v[4:7], v[14:15], off offset:32
	global_load_dwordx4 v[8:11], v[14:15], off offset:16
	s_waitcnt lgkmcnt(1)
	s_waitcnt lgkmcnt(0)
	v_readlane_b32 s15, v90, 63
	v_sub_f32_e32 v90, s15, v90
	s_waitcnt lgkmcnt(1)
	v_mul_f32_e32 v90, 0x3fb8aa3b, v90
	s_waitcnt lgkmcnt(0)
	v_exp_f32_e32 v90, v90
	s_waitcnt lgkmcnt(1)
	s_waitcnt lgkmcnt(1)
	s_waitcnt lgkmcnt(0)
	global_load_dwordx4 v[14:17], v[14:15], off offset:48
	s_waitcnt lgkmcnt(1)
	s_waitcnt lgkmcnt(1)
	v_readlane_b32 vcc_hi, v92, 63
	s_waitcnt lgkmcnt(0)
	s_waitcnt vmcnt(3)
	v_lshlrev_b32_e32 v94, 16, v0
	v_and_b32_e32 v0, 0xffff0000, v0
	v_mul_f32_e32 v0, v91, v0
	v_cvt_pk_bf16_f32 v0, v0, s0
	v_mul_f32_e32 v90, v90, v94
	ds_write_b16 v54, v0 offset:128
	v_sub_f32_e32 v0, vcc_hi, v92
	v_cvt_pk_bf16_f32 v90, v90, s0
	v_mul_f32_e32 v0, 0x3fb8aa3b, v0
	ds_write_b16 v54, v90
	v_exp_f32_e32 v0, v0
	v_sub_f32_e32 v90, s48, v93
	v_mul_f32_e32 v90, 0x3fb8aa3b, v90
	v_exp_f32_e32 v90, v90
	v_lshlrev_b32_e32 v95, 16, v1
	v_mul_f32_e32 v0, v0, v95
	v_and_b32_e32 v1, 0xffff0000, v1
	v_cvt_pk_bf16_f32 v0, v0, s0
	ds_write_b16 v54, v0 offset:256
	v_mul_f32_e32 v0, v90, v1
	v_cvt_pk_bf16_f32 v0, v0, s0
	ds_write_b16 v54, v0 offset:384
	v_sub_f32_e32 v0, s50, v18
	v_mul_f32_e32 v0, 0x3fb8aa3b, v0
	v_readlane_b32 vcc_lo, v19, 63
	v_exp_f32_e32 v0, v0
	v_lshlrev_b32_e32 v96, 16, v2
	v_sub_f32_e32 v1, vcc_lo, v19
	v_mul_f32_e32 v1, 0x3fb8aa3b, v1
	v_exp_f32_e32 v1, v1
	v_mul_f32_e32 v0, v0, v96
	v_and_b32_e32 v2, 0xffff0000, v2
	v_cvt_pk_bf16_f32 v0, v0, s0
	ds_write_b16 v54, v0 offset:512
	v_mul_f32_e32 v0, v1, v2
	v_cvt_pk_bf16_f32 v0, v0, s0
	ds_write_b16 v54, v0 offset:640
	v_sub_f32_e32 v0, s49, v20
	v_mul_f32_e32 v0, 0x3fb8aa3b, v0
	v_exp_f32_e32 v0, v0
	v_sub_f32_e32 v1, s51, v21
	v_mul_f32_e32 v1, 0x3fb8aa3b, v1
	v_exp_f32_e32 v1, v1
	v_lshlrev_b32_e32 v98, 16, v3
	v_mul_f32_e32 v0, v0, v98
	v_and_b32_e32 v3, 0xffff0000, v3
	v_cvt_pk_bf16_f32 v0, v0, s0
	ds_write_b16 v54, v0 offset:768
	v_mul_f32_e32 v0, v1, v3
	v_cvt_pk_bf16_f32 v0, v0, s0
	ds_write_b16 v54, v0 offset:896
	v_sub_f32_e32 v0, s52, v22
	v_mul_f32_e32 v0, 0x3fb8aa3b, v0
	v_exp_f32_e32 v0, v0
	v_sub_f32_e32 v1, s53, v23
	v_mul_f32_e32 v1, 0x3fb8aa3b, v1
	v_exp_f32_e32 v1, v1
	s_waitcnt vmcnt(1)
	v_lshlrev_b32_e32 v99, 16, v8
	v_mul_f32_e32 v0, v0, v99
	v_and_b32_e32 v8, 0xffff0000, v8
	v_cvt_pk_bf16_f32 v0, v0, s0
	ds_write_b16 v54, v0 offset:1024
	v_mul_f32_e32 v0, v1, v8
	v_cvt_pk_bf16_f32 v0, v0, s0
	ds_write_b16 v54, v0 offset:1152
	v_sub_f32_e32 v0, s54, v24
	v_mul_f32_e32 v0, 0x3fb8aa3b, v0
	v_exp_f32_e32 v0, v0
	v_sub_f32_e32 v1, s56, v25
	v_mul_f32_e32 v1, 0x3fb8aa3b, v1
	v_exp_f32_e32 v1, v1
	v_lshlrev_b32_e32 v100, 16, v9
	v_mul_f32_e32 v0, v0, v100
	v_and_b32_e32 v9, 0xffff0000, v9
	v_cvt_pk_bf16_f32 v0, v0, s0
	ds_write_b16 v54, v0 offset:1280
	v_mul_f32_e32 v0, v1, v9
	v_cvt_pk_bf16_f32 v0, v0, s0
	ds_write_b16 v54, v0 offset:1408
	v_sub_f32_e32 v0, s55, v26
	v_mul_f32_e32 v0, 0x3fb8aa3b, v0
	v_exp_f32_e32 v0, v0
	v_sub_f32_e32 v1, s57, v27
	v_mul_f32_e32 v1, 0x3fb8aa3b, v1
	v_exp_f32_e32 v1, v1
	v_lshlrev_b32_e32 v101, 16, v10
	v_mul_f32_e32 v0, v0, v101
	v_and_b32_e32 v10, 0xffff0000, v10
	v_cvt_pk_bf16_f32 v0, v0, s0
	ds_write_b16 v54, v0 offset:1536
	v_mul_f32_e32 v0, v1, v10
	v_cvt_pk_bf16_f32 v0, v0, s0
	ds_write_b16 v54, v0 offset:1664
	v_sub_f32_e32 v0, s58, v28
	v_mul_f32_e32 v0, 0x3fb8aa3b, v0
	v_exp_f32_e32 v0, v0
	v_sub_f32_e32 v1, s59, v29
	v_mul_f32_e32 v1, 0x3fb8aa3b, v1
	v_exp_f32_e32 v1, v1
	v_lshlrev_b32_e32 v102, 16, v11
	v_mul_f32_e32 v0, v0, v102
	v_and_b32_e32 v11, 0xffff0000, v11
	v_cvt_pk_bf16_f32 v0, v0, s0
	ds_write_b16 v54, v0 offset:1792
	v_mul_f32_e32 v0, v1, v11
	v_cvt_pk_bf16_f32 v0, v0, s0
	ds_write_b16 v54, v0 offset:1920
	v_sub_f32_e32 v0, s60, v30
	v_mul_f32_e32 v0, 0x3fb8aa3b, v0
	v_exp_f32_e32 v0, v0
	v_sub_f32_e32 v1, s61, v31
	v_mul_f32_e32 v1, 0x3fb8aa3b, v1
	v_exp_f32_e32 v1, v1
	v_lshlrev_b32_e32 v103, 16, v4
	v_mul_f32_e32 v0, v0, v103
	v_and_b32_e32 v4, 0xffff0000, v4
	v_cvt_pk_bf16_f32 v0, v0, s0
	ds_write_b16 v54, v0 offset:2048
	v_mul_f32_e32 v0, v1, v4
	v_cvt_pk_bf16_f32 v0, v0, s0
	ds_write_b16 v54, v0 offset:2176
	v_sub_f32_e32 v0, s62, v76
	v_mul_f32_e32 v0, 0x3fb8aa3b, v0
	v_exp_f32_e32 v0, v0
	v_sub_f32_e32 v1, s63, v77
	v_mul_f32_e32 v1, 0x3fb8aa3b, v1
	v_exp_f32_e32 v1, v1
	v_lshlrev_b32_e32 v104, 16, v5
	v_mul_f32_e32 v0, v0, v104
	v_and_b32_e32 v5, 0xffff0000, v5
	v_cvt_pk_bf16_f32 v0, v0, s0
	ds_write_b16 v54, v0 offset:2304
	v_mul_f32_e32 v0, v1, v5
	v_cvt_pk_bf16_f32 v0, v0, s0
	v_readlane_b32 s64, v78, 63
	ds_write_b16 v54, v0 offset:2432
	v_readlane_b32 s65, v79, 63
	v_sub_f32_e32 v0, s64, v78
	v_mul_f32_e32 v0, 0x3fb8aa3b, v0
	v_exp_f32_e32 v0, v0
	v_sub_f32_e32 v1, s65, v79
	v_mul_f32_e32 v1, 0x3fb8aa3b, v1
	v_exp_f32_e32 v1, v1
	v_lshlrev_b32_e32 v105, 16, v6
	v_mul_f32_e32 v0, v0, v105
	v_and_b32_e32 v6, 0xffff0000, v6
	v_cvt_pk_bf16_f32 v0, v0, s0
	ds_write_b16 v54, v0 offset:2560
	v_mul_f32_e32 v0, v1, v6
	v_cvt_pk_bf16_f32 v0, v0, s0
	v_readlane_b32 s66, v81, 63
	ds_write_b16 v54, v0 offset:2688
	v_readlane_b32 s67, v82, 63
	v_sub_f32_e32 v0, s66, v81
	v_mul_f32_e32 v0, 0x3fb8aa3b, v0
	v_exp_f32_e32 v0, v0
	v_sub_f32_e32 v1, s67, v82
	v_mul_f32_e32 v1, 0x3fb8aa3b, v1
	v_exp_f32_e32 v1, v1
	v_lshlrev_b32_e32 v106, 16, v7
	v_mul_f32_e32 v0, v0, v106
	v_and_b32_e32 v7, 0xffff0000, v7
	v_cvt_pk_bf16_f32 v0, v0, s0
	ds_write_b16 v54, v0 offset:2816
	v_mul_f32_e32 v0, v1, v7
	v_cvt_pk_bf16_f32 v0, v0, s0
	v_readlane_b32 s68, v80, 63
	ds_write_b16 v54, v0 offset:2944
	v_readlane_b32 s69, v83, 63
	v_sub_f32_e32 v0, s68, v80
	v_mul_f32_e32 v0, 0x3fb8aa3b, v0
	v_exp_f32_e32 v0, v0
	v_sub_f32_e32 v1, s69, v83
	v_mul_f32_e32 v1, 0x3fb8aa3b, v1
	v_exp_f32_e32 v1, v1
	s_waitcnt vmcnt(0)
	v_lshlrev_b32_e32 v107, 16, v14
	v_mul_f32_e32 v0, v0, v107
	v_and_b32_e32 v14, 0xffff0000, v14
	v_cvt_pk_bf16_f32 v0, v0, s0
	ds_write_b16 v54, v0 offset:3072
	v_mul_f32_e32 v0, v1, v14
	v_cvt_pk_bf16_f32 v0, v0, s0
	v_readlane_b32 s70, v84, 63
	ds_write_b16 v54, v0 offset:3200
	v_readlane_b32 s71, v85, 63
	v_sub_f32_e32 v0, s70, v84
	v_mul_f32_e32 v0, 0x3fb8aa3b, v0
	v_exp_f32_e32 v0, v0
	v_sub_f32_e32 v1, s71, v85
	v_mul_f32_e32 v1, 0x3fb8aa3b, v1
	v_exp_f32_e32 v1, v1
	v_lshlrev_b32_e32 v108, 16, v15
	v_mul_f32_e32 v0, v0, v108
	v_and_b32_e32 v15, 0xffff0000, v15
	v_cvt_pk_bf16_f32 v0, v0, s0
	ds_write_b16 v54, v0 offset:3328
	v_mul_f32_e32 v0, v1, v15
	v_cvt_pk_bf16_f32 v0, v0, s0
	v_readlane_b32 s72, v86, 63
	ds_write_b16 v54, v0 offset:3456
	v_readlane_b32 s73, v87, 63
	v_sub_f32_e32 v0, s72, v86
	v_mul_f32_e32 v0, 0x3fb8aa3b, v0
	v_exp_f32_e32 v0, v0
	v_sub_f32_e32 v1, s73, v87
	v_mul_f32_e32 v1, 0x3fb8aa3b, v1
	v_exp_f32_e32 v1, v1
	v_lshlrev_b32_e32 v109, 16, v16
	v_mul_f32_e32 v0, v0, v109
	v_and_b32_e32 v16, 0xffff0000, v16
	v_cvt_pk_bf16_f32 v0, v0, s0
	ds_write_b16 v54, v0 offset:3584
	v_mul_f32_e32 v0, v1, v16
	v_cvt_pk_bf16_f32 v0, v0, s0
	v_readlane_b32 s74, v88, 63
	ds_write_b16 v54, v0 offset:3712
	v_readlane_b32 s75, v89, 63
	v_sub_f32_e32 v0, s74, v88
	v_mul_f32_e32 v0, 0x3fb8aa3b, v0
	v_exp_f32_e32 v0, v0
	v_sub_f32_e32 v1, s75, v89
	v_mul_f32_e32 v1, 0x3fb8aa3b, v1
	v_exp_f32_e32 v1, v1
	v_lshlrev_b32_e32 v110, 16, v17
	v_mul_f32_e32 v0, v0, v110
	v_and_b32_e32 v17, 0xffff0000, v17
	v_cvt_pk_bf16_f32 v0, v0, s0
	ds_write_b16 v54, v0 offset:3840
	v_mul_f32_e32 v0, v1, v17
	v_cvt_pk_bf16_f32 v0, v0, s0
	ds_write_b16 v54, v0 offset:3968
	s_and_saveexec_b64 s[30:31], s[46:47]
	s_cbranch_execz .LBB0_346
	v_mov_b32_e32 v0, s15
	v_cndmask_b32_e64 v0, 0, v0, s[38:39]
	v_mov_b32_e32 v1, s19
	v_cndmask_b32_e64 v0, v0, v1, s[12:13]
	v_mov_b32_e32 v1, vcc_hi
	v_cndmask_b32_e64 v0, v0, v1, s[10:11]
	v_mov_b32_e32 v1, s48
	v_cndmask_b32_e64 v0, v0, v1, s[8:9]
	v_mov_b32_e32 v1, s50
	v_cndmask_b32_e64 v0, v0, v1, s[6:7]
	v_mov_b32_e32 v1, vcc_lo
	v_cndmask_b32_e64 v0, v0, v1, s[4:5]
	v_mov_b32_e32 v1, s49
	v_cndmask_b32_e64 v0, v0, v1, s[2:3]
	v_mov_b32_e32 v1, s51
	v_cndmask_b32_e64 v0, v0, v1, s[96:97]
	v_mov_b32_e32 v1, s52
	v_cndmask_b32_e64 v0, v0, v1, s[94:95]
	v_mov_b32_e32 v1, s53
	v_cndmask_b32_e64 v0, v0, v1, s[92:93]
	v_mov_b32_e32 v1, s54
	v_cndmask_b32_e64 v0, v0, v1, s[90:91]
	v_mov_b32_e32 v1, s56
	v_cndmask_b32_e64 v0, v0, v1, s[88:89]
	v_mov_b32_e32 v1, s55
	v_cndmask_b32_e64 v0, v0, v1, s[78:79]
	v_mov_b32_e32 v1, s57
	v_cndmask_b32_e64 v0, v0, v1, s[84:85]
	v_mov_b32_e32 v1, s58
	v_cndmask_b32_e64 v0, v0, v1, s[82:83]
	v_mov_b32_e32 v1, s59
	v_readlane_b32 s48, v255, 11
	v_cndmask_b32_e64 v0, v0, v1, s[80:81]
	v_mov_b32_e32 v1, s60
	v_readlane_b32 s49, v255, 12
	s_nop 1
	v_cndmask_b32_e64 v0, v0, v1, s[48:49]
	v_readlane_b32 s48, v255, 9
	v_mov_b32_e32 v1, s61
	v_readlane_b32 s49, v255, 10
	s_nop 1
	v_cndmask_b32_e64 v0, v0, v1, s[48:49]
	v_readlane_b32 s48, v255, 7
	v_mov_b32_e32 v1, s62
	v_readlane_b32 s49, v255, 8
	s_nop 1
	v_cndmask_b32_e64 v0, v0, v1, s[48:49]
	v_readlane_b32 s48, v255, 5
	v_mov_b32_e32 v1, s63
	v_readlane_b32 s49, v255, 6
	s_nop 1
	v_cndmask_b32_e64 v0, v0, v1, s[48:49]
	v_readlane_b32 s48, v255, 3
	v_mov_b32_e32 v1, s64
	v_readlane_b32 s49, v255, 4
	s_nop 1
	v_cndmask_b32_e64 v0, v0, v1, s[48:49]
	v_readlane_b32 s48, v255, 1
	v_mov_b32_e32 v1, s65
	v_readlane_b32 s49, v255, 2
	s_nop 1
	v_cndmask_b32_e64 v0, v0, v1, s[48:49]
	v_readlane_b32 s48, v254, 63
	v_mov_b32_e32 v1, s66
	v_readlane_b32 s49, v255, 0
	s_nop 1
	v_cndmask_b32_e64 v0, v0, v1, s[48:49]
	v_readlane_b32 s48, v254, 61
	v_mov_b32_e32 v1, s67
	v_readlane_b32 s49, v254, 62
	s_nop 1
	v_cndmask_b32_e64 v0, v0, v1, s[48:49]
	v_readlane_b32 s48, v254, 59
	v_mov_b32_e32 v1, s68
	v_readlane_b32 s49, v254, 60
	s_nop 1
	v_cndmask_b32_e64 v0, v0, v1, s[48:49]
	v_readlane_b32 s48, v254, 57
	v_mov_b32_e32 v1, s69
	v_readlane_b32 s49, v254, 58
	s_nop 1
	v_cndmask_b32_e64 v0, v0, v1, s[48:49]
	v_readlane_b32 s48, v254, 55
	v_mov_b32_e32 v1, s70
	v_readlane_b32 s49, v254, 56
	s_nop 1
	v_cndmask_b32_e64 v0, v0, v1, s[48:49]
	v_readlane_b32 s48, v254, 53
	v_mov_b32_e32 v1, s71
	v_readlane_b32 s49, v254, 54
	s_nop 1
	v_cndmask_b32_e64 v0, v0, v1, s[48:49]
	v_readlane_b32 s48, v254, 51
	v_mov_b32_e32 v1, s72
	v_readlane_b32 s49, v254, 52
	s_nop 1
	v_cndmask_b32_e64 v0, v0, v1, s[48:49]
	v_readlane_b32 s48, v254, 49
	v_mov_b32_e32 v1, s73
	v_readlane_b32 s49, v254, 50
	s_nop 1
	v_cndmask_b32_e64 v0, v0, v1, s[48:49]
	v_readlane_b32 s48, v254, 47
	v_mov_b32_e32 v1, s74
	v_readlane_b32 s49, v254, 48
	s_nop 1
	v_cndmask_b32_e64 v0, v0, v1, s[48:49]
	v_readlane_b32 s48, v254, 45
	v_mov_b32_e32 v1, s75
	v_readlane_b32 s49, v254, 46
	s_nop 1
	v_cndmask_b32_e64 v2, v0, v1, s[48:49]
	v_mul_f32_e32 v2, 0x3fb8aa3b, v2
	v_exp_f32_e32 v2, v2
	v_lshl_or_b32 v0, s14, 7, v55
	v_ashrrev_i32_e32 v1, 31, v0
	v_lshl_add_u64 v[0:1], v[0:1], 2, s[24:25]
	global_store_dword v[0:1], v2, off
	s_branch .LBB0_346

.LBB0_768:
	s_ashr_i32 s2, s16, 2
	s_ashr_i32 s3, s2, 31
	s_lshl_b64 s[14:15], s[2:3], 6
	v_mov_b32_e32 v1, s15
	v_or_b32_e32 v0, s14, v100
	v_lshlrev_b64 v[28:29], 9, v[0:1]
	v_lshl_add_u64 v[12:13], s[6:7], 0, v[28:29]
	global_load_dwordx4 v[16:19], v[12:13], off offset:48
	global_load_dwordx4 v[20:23], v[12:13], off offset:32
	global_load_dwordx4 v[24:27], v[12:13], off offset:16
	global_load_dwordx4 v[30:33], v[12:13], off
	global_load_dwordx4 v[0:3], v[12:13], off offset:112
	global_load_dwordx4 v[4:7], v[12:13], off offset:96
	global_load_dwordx4 v[8:11], v[12:13], off offset:80
	s_nop 0
	global_load_dwordx4 v[12:15], v[12:13], off offset:64
	s_waitcnt vmcnt(0)
	s_nop 1
	v_add_f32_dpp v30, v30, v30 row_shr:1 row_mask:0xf bank_mask:0xf bound_ctrl:0
	v_add_f32_dpp v31, v31, v31 row_shr:1 row_mask:0xf bank_mask:0xf bound_ctrl:0
	v_add_f32_dpp v32, v32, v32 row_shr:1 row_mask:0xf bank_mask:0xf bound_ctrl:0
	v_add_f32_dpp v33, v33, v33 row_shr:1 row_mask:0xf bank_mask:0xf bound_ctrl:0
	v_add_f32_dpp v24, v24, v24 row_shr:1 row_mask:0xf bank_mask:0xf bound_ctrl:0
	v_add_f32_dpp v25, v25, v25 row_shr:1 row_mask:0xf bank_mask:0xf bound_ctrl:0
	v_add_f32_dpp v26, v26, v26 row_shr:1 row_mask:0xf bank_mask:0xf bound_ctrl:0
	v_add_f32_dpp v27, v27, v27 row_shr:1 row_mask:0xf bank_mask:0xf bound_ctrl:0
	v_add_f32_dpp v30, v30, v30 row_shr:2 row_mask:0xf bank_mask:0xf bound_ctrl:0
	v_add_f32_dpp v31, v31, v31 row_shr:2 row_mask:0xf bank_mask:0xf bound_ctrl:0
	v_add_f32_dpp v32, v32, v32 row_shr:2 row_mask:0xf bank_mask:0xf bound_ctrl:0
	v_add_f32_dpp v33, v33, v33 row_shr:2 row_mask:0xf bank_mask:0xf bound_ctrl:0
	v_add_f32_dpp v24, v24, v24 row_shr:2 row_mask:0xf bank_mask:0xf bound_ctrl:0
	v_add_f32_dpp v25, v25, v25 row_shr:2 row_mask:0xf bank_mask:0xf bound_ctrl:0
	v_add_f32_dpp v26, v26, v26 row_shr:2 row_mask:0xf bank_mask:0xf bound_ctrl:0
	v_add_f32_dpp v27, v27, v27 row_shr:2 row_mask:0xf bank_mask:0xf bound_ctrl:0
	v_add_f32_dpp v30, v30, v30 row_shr:4 row_mask:0xf bank_mask:0xf bound_ctrl:0
	v_add_f32_dpp v31, v31, v31 row_shr:4 row_mask:0xf bank_mask:0xf bound_ctrl:0
	v_add_f32_dpp v32, v32, v32 row_shr:4 row_mask:0xf bank_mask:0xf bound_ctrl:0
	v_add_f32_dpp v33, v33, v33 row_shr:4 row_mask:0xf bank_mask:0xf bound_ctrl:0
	v_add_f32_dpp v24, v24, v24 row_shr:4 row_mask:0xf bank_mask:0xf bound_ctrl:0
	v_add_f32_dpp v25, v25, v25 row_shr:4 row_mask:0xf bank_mask:0xf bound_ctrl:0
	v_add_f32_dpp v26, v26, v26 row_shr:4 row_mask:0xf bank_mask:0xf bound_ctrl:0
	v_add_f32_dpp v27, v27, v27 row_shr:4 row_mask:0xf bank_mask:0xf bound_ctrl:0
	v_add_f32_dpp v30, v30, v30 row_shr:8 row_mask:0xf bank_mask:0xf bound_ctrl:0
	v_add_f32_dpp v31, v31, v31 row_shr:8 row_mask:0xf bank_mask:0xf bound_ctrl:0
	v_add_f32_dpp v32, v32, v32 row_shr:8 row_mask:0xf bank_mask:0xf bound_ctrl:0
	v_add_f32_dpp v33, v33, v33 row_shr:8 row_mask:0xf bank_mask:0xf bound_ctrl:0
	v_add_f32_dpp v24, v24, v24 row_shr:8 row_mask:0xf bank_mask:0xf bound_ctrl:0
	v_add_f32_dpp v25, v25, v25 row_shr:8 row_mask:0xf bank_mask:0xf bound_ctrl:0
	v_add_f32_dpp v26, v26, v26 row_shr:8 row_mask:0xf bank_mask:0xf bound_ctrl:0
	v_add_f32_dpp v27, v27, v27 row_shr:8 row_mask:0xf bank_mask:0xf bound_ctrl:0
	v_add_f32_dpp v30, v30, v30 row_bcast:15 row_mask:0xa bank_mask:0xf
	v_add_f32_dpp v31, v31, v31 row_bcast:15 row_mask:0xa bank_mask:0xf
	v_add_f32_dpp v32, v32, v32 row_bcast:15 row_mask:0xa bank_mask:0xf
	v_add_f32_dpp v33, v33, v33 row_bcast:15 row_mask:0xa bank_mask:0xf
	v_add_f32_dpp v24, v24, v24 row_bcast:15 row_mask:0xa bank_mask:0xf
	v_add_f32_dpp v25, v25, v25 row_bcast:15 row_mask:0xa bank_mask:0xf
	v_add_f32_dpp v26, v26, v26 row_bcast:15 row_mask:0xa bank_mask:0xf
	v_add_f32_dpp v27, v27, v27 row_bcast:15 row_mask:0xa bank_mask:0xf
	v_add_f32_dpp v30, v30, v30 row_bcast:31 row_mask:0xc bank_mask:0xf
	v_add_f32_dpp v31, v31, v31 row_bcast:31 row_mask:0xc bank_mask:0xf
	v_add_f32_dpp v32, v32, v32 row_bcast:31 row_mask:0xc bank_mask:0xf
	v_add_f32_dpp v33, v33, v33 row_bcast:31 row_mask:0xc bank_mask:0xf
	v_add_f32_dpp v24, v24, v24 row_bcast:31 row_mask:0xc bank_mask:0xf
	v_add_f32_dpp v25, v25, v25 row_bcast:31 row_mask:0xc bank_mask:0xf
	v_add_f32_dpp v26, v26, v26 row_bcast:31 row_mask:0xc bank_mask:0xf
	v_add_f32_dpp v27, v27, v27 row_bcast:31 row_mask:0xc bank_mask:0xf
	v_add_f32_dpp v20, v20, v20 row_shr:1 row_mask:0xf bank_mask:0xf bound_ctrl:0
	v_add_f32_dpp v21, v21, v21 row_shr:1 row_mask:0xf bank_mask:0xf bound_ctrl:0
	v_add_f32_dpp v22, v22, v22 row_shr:1 row_mask:0xf bank_mask:0xf bound_ctrl:0
	v_add_f32_dpp v23, v23, v23 row_shr:1 row_mask:0xf bank_mask:0xf bound_ctrl:0
	v_add_f32_dpp v16, v16, v16 row_shr:1 row_mask:0xf bank_mask:0xf bound_ctrl:0
	v_add_f32_dpp v17, v17, v17 row_shr:1 row_mask:0xf bank_mask:0xf bound_ctrl:0
	v_add_f32_dpp v18, v18, v18 row_shr:1 row_mask:0xf bank_mask:0xf bound_ctrl:0
	v_add_f32_dpp v19, v19, v19 row_shr:1 row_mask:0xf bank_mask:0xf bound_ctrl:0
	v_add_f32_dpp v20, v20, v20 row_shr:2 row_mask:0xf bank_mask:0xf bound_ctrl:0
	v_add_f32_dpp v21, v21, v21 row_shr:2 row_mask:0xf bank_mask:0xf bound_ctrl:0
	v_add_f32_dpp v22, v22, v22 row_shr:2 row_mask:0xf bank_mask:0xf bound_ctrl:0
	v_add_f32_dpp v23, v23, v23 row_shr:2 row_mask:0xf bank_mask:0xf bound_ctrl:0
	v_add_f32_dpp v16, v16, v16 row_shr:2 row_mask:0xf bank_mask:0xf bound_ctrl:0
	v_add_f32_dpp v17, v17, v17 row_shr:2 row_mask:0xf bank_mask:0xf bound_ctrl:0
	v_add_f32_dpp v18, v18, v18 row_shr:2 row_mask:0xf bank_mask:0xf bound_ctrl:0
	v_add_f32_dpp v19, v19, v19 row_shr:2 row_mask:0xf bank_mask:0xf bound_ctrl:0
	v_add_f32_dpp v20, v20, v20 row_shr:4 row_mask:0xf bank_mask:0xf bound_ctrl:0
	v_add_f32_dpp v21, v21, v21 row_shr:4 row_mask:0xf bank_mask:0xf bound_ctrl:0
	v_add_f32_dpp v22, v22, v22 row_shr:4 row_mask:0xf bank_mask:0xf bound_ctrl:0
	v_add_f32_dpp v23, v23, v23 row_shr:4 row_mask:0xf bank_mask:0xf bound_ctrl:0
	v_add_f32_dpp v16, v16, v16 row_shr:4 row_mask:0xf bank_mask:0xf bound_ctrl:0
	v_add_f32_dpp v17, v17, v17 row_shr:4 row_mask:0xf bank_mask:0xf bound_ctrl:0
	v_add_f32_dpp v18, v18, v18 row_shr:4 row_mask:0xf bank_mask:0xf bound_ctrl:0
	v_add_f32_dpp v19, v19, v19 row_shr:4 row_mask:0xf bank_mask:0xf bound_ctrl:0
	v_add_f32_dpp v20, v20, v20 row_shr:8 row_mask:0xf bank_mask:0xf bound_ctrl:0
	v_add_f32_dpp v21, v21, v21 row_shr:8 row_mask:0xf bank_mask:0xf bound_ctrl:0
	v_add_f32_dpp v22, v22, v22 row_shr:8 row_mask:0xf bank_mask:0xf bound_ctrl:0
	v_add_f32_dpp v23, v23, v23 row_shr:8 row_mask:0xf bank_mask:0xf bound_ctrl:0
	v_add_f32_dpp v16, v16, v16 row_shr:8 row_mask:0xf bank_mask:0xf bound_ctrl:0
	v_add_f32_dpp v17, v17, v17 row_shr:8 row_mask:0xf bank_mask:0xf bound_ctrl:0
	v_add_f32_dpp v18, v18, v18 row_shr:8 row_mask:0xf bank_mask:0xf bound_ctrl:0
	v_add_f32_dpp v19, v19, v19 row_shr:8 row_mask:0xf bank_mask:0xf bound_ctrl:0
	v_add_f32_dpp v20, v20, v20 row_bcast:15 row_mask:0xa bank_mask:0xf
	v_add_f32_dpp v21, v21, v21 row_bcast:15 row_mask:0xa bank_mask:0xf
	v_add_f32_dpp v22, v22, v22 row_bcast:15 row_mask:0xa bank_mask:0xf
	v_add_f32_dpp v23, v23, v23 row_bcast:15 row_mask:0xa bank_mask:0xf
	v_add_f32_dpp v16, v16, v16 row_bcast:15 row_mask:0xa bank_mask:0xf
	v_add_f32_dpp v17, v17, v17 row_bcast:15 row_mask:0xa bank_mask:0xf
	v_add_f32_dpp v18, v18, v18 row_bcast:15 row_mask:0xa bank_mask:0xf
	v_add_f32_dpp v19, v19, v19 row_bcast:15 row_mask:0xa bank_mask:0xf
	v_add_f32_dpp v20, v20, v20 row_bcast:31 row_mask:0xc bank_mask:0xf
	v_add_f32_dpp v21, v21, v21 row_bcast:31 row_mask:0xc bank_mask:0xf
	v_add_f32_dpp v22, v22, v22 row_bcast:31 row_mask:0xc bank_mask:0xf
	v_add_f32_dpp v23, v23, v23 row_bcast:31 row_mask:0xc bank_mask:0xf
	v_add_f32_dpp v16, v16, v16 row_bcast:31 row_mask:0xc bank_mask:0xf
	v_add_f32_dpp v17, v17, v17 row_bcast:31 row_mask:0xc bank_mask:0xf
	v_add_f32_dpp v18, v18, v18 row_bcast:31 row_mask:0xc bank_mask:0xf
	v_add_f32_dpp v19, v19, v19 row_bcast:31 row_mask:0xc bank_mask:0xf
	v_add_f32_dpp v12, v12, v12 row_shr:1 row_mask:0xf bank_mask:0xf bound_ctrl:0
	v_add_f32_dpp v13, v13, v13 row_shr:1 row_mask:0xf bank_mask:0xf bound_ctrl:0
	v_add_f32_dpp v14, v14, v14 row_shr:1 row_mask:0xf bank_mask:0xf bound_ctrl:0
	v_add_f32_dpp v15, v15, v15 row_shr:1 row_mask:0xf bank_mask:0xf bound_ctrl:0
	v_add_f32_dpp v8, v8, v8 row_shr:1 row_mask:0xf bank_mask:0xf bound_ctrl:0
	v_add_f32_dpp v9, v9, v9 row_shr:1 row_mask:0xf bank_mask:0xf bound_ctrl:0
	v_add_f32_dpp v10, v10, v10 row_shr:1 row_mask:0xf bank_mask:0xf bound_ctrl:0
	v_add_f32_dpp v11, v11, v11 row_shr:1 row_mask:0xf bank_mask:0xf bound_ctrl:0
	v_add_f32_dpp v12, v12, v12 row_shr:2 row_mask:0xf bank_mask:0xf bound_ctrl:0
	v_add_f32_dpp v13, v13, v13 row_shr:2 row_mask:0xf bank_mask:0xf bound_ctrl:0
	v_add_f32_dpp v14, v14, v14 row_shr:2 row_mask:0xf bank_mask:0xf bound_ctrl:0
	v_add_f32_dpp v15, v15, v15 row_shr:2 row_mask:0xf bank_mask:0xf bound_ctrl:0
	v_add_f32_dpp v8, v8, v8 row_shr:2 row_mask:0xf bank_mask:0xf bound_ctrl:0
	v_add_f32_dpp v9, v9, v9 row_shr:2 row_mask:0xf bank_mask:0xf bound_ctrl:0
	v_add_f32_dpp v10, v10, v10 row_shr:2 row_mask:0xf bank_mask:0xf bound_ctrl:0
	v_add_f32_dpp v11, v11, v11 row_shr:2 row_mask:0xf bank_mask:0xf bound_ctrl:0
	v_add_f32_dpp v12, v12, v12 row_shr:4 row_mask:0xf bank_mask:0xf bound_ctrl:0
	v_add_f32_dpp v13, v13, v13 row_shr:4 row_mask:0xf bank_mask:0xf bound_ctrl:0
	v_add_f32_dpp v14, v14, v14 row_shr:4 row_mask:0xf bank_mask:0xf bound_ctrl:0
	v_add_f32_dpp v15, v15, v15 row_shr:4 row_mask:0xf bank_mask:0xf bound_ctrl:0
	v_add_f32_dpp v8, v8, v8 row_shr:4 row_mask:0xf bank_mask:0xf bound_ctrl:0
	v_add_f32_dpp v9, v9, v9 row_shr:4 row_mask:0xf bank_mask:0xf bound_ctrl:0
	v_add_f32_dpp v10, v10, v10 row_shr:4 row_mask:0xf bank_mask:0xf bound_ctrl:0
	v_add_f32_dpp v11, v11, v11 row_shr:4 row_mask:0xf bank_mask:0xf bound_ctrl:0
	v_add_f32_dpp v12, v12, v12 row_shr:8 row_mask:0xf bank_mask:0xf bound_ctrl:0
	v_add_f32_dpp v13, v13, v13 row_shr:8 row_mask:0xf bank_mask:0xf bound_ctrl:0
	v_add_f32_dpp v14, v14, v14 row_shr:8 row_mask:0xf bank_mask:0xf bound_ctrl:0
	v_add_f32_dpp v15, v15, v15 row_shr:8 row_mask:0xf bank_mask:0xf bound_ctrl:0
	v_add_f32_dpp v8, v8, v8 row_shr:8 row_mask:0xf bank_mask:0xf bound_ctrl:0
	v_add_f32_dpp v9, v9, v9 row_shr:8 row_mask:0xf bank_mask:0xf bound_ctrl:0
	v_add_f32_dpp v10, v10, v10 row_shr:8 row_mask:0xf bank_mask:0xf bound_ctrl:0
	v_add_f32_dpp v11, v11, v11 row_shr:8 row_mask:0xf bank_mask:0xf bound_ctrl:0
	v_add_f32_dpp v12, v12, v12 row_bcast:15 row_mask:0xa bank_mask:0xf
	v_add_f32_dpp v13, v13, v13 row_bcast:15 row_mask:0xa bank_mask:0xf
	v_add_f32_dpp v14, v14, v14 row_bcast:15 row_mask:0xa bank_mask:0xf
	v_add_f32_dpp v15, v15, v15 row_bcast:15 row_mask:0xa bank_mask:0xf
	v_add_f32_dpp v8, v8, v8 row_bcast:15 row_mask:0xa bank_mask:0xf
	v_add_f32_dpp v9, v9, v9 row_bcast:15 row_mask:0xa bank_mask:0xf
	v_add_f32_dpp v10, v10, v10 row_bcast:15 row_mask:0xa bank_mask:0xf
	v_add_f32_dpp v11, v11, v11 row_bcast:15 row_mask:0xa bank_mask:0xf
	v_add_f32_dpp v12, v12, v12 row_bcast:31 row_mask:0xc bank_mask:0xf
	v_add_f32_dpp v13, v13, v13 row_bcast:31 row_mask:0xc bank_mask:0xf
	v_add_f32_dpp v14, v14, v14 row_bcast:31 row_mask:0xc bank_mask:0xf
	v_add_f32_dpp v15, v15, v15 row_bcast:31 row_mask:0xc bank_mask:0xf
	v_add_f32_dpp v8, v8, v8 row_bcast:31 row_mask:0xc bank_mask:0xf
	v_add_f32_dpp v9, v9, v9 row_bcast:31 row_mask:0xc bank_mask:0xf
	v_add_f32_dpp v10, v10, v10 row_bcast:31 row_mask:0xc bank_mask:0xf
	v_add_f32_dpp v11, v11, v11 row_bcast:31 row_mask:0xc bank_mask:0xf
	v_add_f32_dpp v4, v4, v4 row_shr:1 row_mask:0xf bank_mask:0xf bound_ctrl:0
	v_add_f32_dpp v5, v5, v5 row_shr:1 row_mask:0xf bank_mask:0xf bound_ctrl:0
	v_add_f32_dpp v6, v6, v6 row_shr:1 row_mask:0xf bank_mask:0xf bound_ctrl:0
	v_add_f32_dpp v7, v7, v7 row_shr:1 row_mask:0xf bank_mask:0xf bound_ctrl:0
	v_add_f32_dpp v0, v0, v0 row_shr:1 row_mask:0xf bank_mask:0xf bound_ctrl:0
	v_add_f32_dpp v1, v1, v1 row_shr:1 row_mask:0xf bank_mask:0xf bound_ctrl:0
	v_add_f32_dpp v2, v2, v2 row_shr:1 row_mask:0xf bank_mask:0xf bound_ctrl:0
	v_add_f32_dpp v3, v3, v3 row_shr:1 row_mask:0xf bank_mask:0xf bound_ctrl:0
	v_add_f32_dpp v4, v4, v4 row_shr:2 row_mask:0xf bank_mask:0xf bound_ctrl:0
	v_add_f32_dpp v5, v5, v5 row_shr:2 row_mask:0xf bank_mask:0xf bound_ctrl:0
	v_add_f32_dpp v6, v6, v6 row_shr:2 row_mask:0xf bank_mask:0xf bound_ctrl:0
	v_add_f32_dpp v7, v7, v7 row_shr:2 row_mask:0xf bank_mask:0xf bound_ctrl:0
	v_add_f32_dpp v0, v0, v0 row_shr:2 row_mask:0xf bank_mask:0xf bound_ctrl:0
	v_add_f32_dpp v1, v1, v1 row_shr:2 row_mask:0xf bank_mask:0xf bound_ctrl:0
	v_add_f32_dpp v2, v2, v2 row_shr:2 row_mask:0xf bank_mask:0xf bound_ctrl:0
	v_add_f32_dpp v3, v3, v3 row_shr:2 row_mask:0xf bank_mask:0xf bound_ctrl:0
	v_add_f32_dpp v4, v4, v4 row_shr:4 row_mask:0xf bank_mask:0xf bound_ctrl:0
	v_add_f32_dpp v5, v5, v5 row_shr:4 row_mask:0xf bank_mask:0xf bound_ctrl:0
	v_add_f32_dpp v6, v6, v6 row_shr:4 row_mask:0xf bank_mask:0xf bound_ctrl:0
	v_add_f32_dpp v7, v7, v7 row_shr:4 row_mask:0xf bank_mask:0xf bound_ctrl:0
	v_add_f32_dpp v0, v0, v0 row_shr:4 row_mask:0xf bank_mask:0xf bound_ctrl:0
	v_add_f32_dpp v1, v1, v1 row_shr:4 row_mask:0xf bank_mask:0xf bound_ctrl:0
	v_add_f32_dpp v2, v2, v2 row_shr:4 row_mask:0xf bank_mask:0xf bound_ctrl:0
	v_add_f32_dpp v3, v3, v3 row_shr:4 row_mask:0xf bank_mask:0xf bound_ctrl:0
	v_add_f32_dpp v4, v4, v4 row_shr:8 row_mask:0xf bank_mask:0xf bound_ctrl:0
	v_add_f32_dpp v5, v5, v5 row_shr:8 row_mask:0xf bank_mask:0xf bound_ctrl:0
	v_add_f32_dpp v6, v6, v6 row_shr:8 row_mask:0xf bank_mask:0xf bound_ctrl:0
	v_add_f32_dpp v7, v7, v7 row_shr:8 row_mask:0xf bank_mask:0xf bound_ctrl:0
	v_add_f32_dpp v0, v0, v0 row_shr:8 row_mask:0xf bank_mask:0xf bound_ctrl:0
	v_add_f32_dpp v1, v1, v1 row_shr:8 row_mask:0xf bank_mask:0xf bound_ctrl:0
	v_add_f32_dpp v2, v2, v2 row_shr:8 row_mask:0xf bank_mask:0xf bound_ctrl:0
	v_add_f32_dpp v3, v3, v3 row_shr:8 row_mask:0xf bank_mask:0xf bound_ctrl:0
	v_add_f32_dpp v4, v4, v4 row_bcast:15 row_mask:0xa bank_mask:0xf
	v_add_f32_dpp v5, v5, v5 row_bcast:15 row_mask:0xa bank_mask:0xf
	v_add_f32_dpp v6, v6, v6 row_bcast:15 row_mask:0xa bank_mask:0xf
	v_add_f32_dpp v7, v7, v7 row_bcast:15 row_mask:0xa bank_mask:0xf
	v_add_f32_dpp v0, v0, v0 row_bcast:15 row_mask:0xa bank_mask:0xf
	v_add_f32_dpp v1, v1, v1 row_bcast:15 row_mask:0xa bank_mask:0xf
	v_add_f32_dpp v2, v2, v2 row_bcast:15 row_mask:0xa bank_mask:0xf
	v_add_f32_dpp v3, v3, v3 row_bcast:15 row_mask:0xa bank_mask:0xf
	v_add_f32_dpp v4, v4, v4 row_bcast:31 row_mask:0xc bank_mask:0xf
	v_add_f32_dpp v5, v5, v5 row_bcast:31 row_mask:0xc bank_mask:0xf
	v_add_f32_dpp v6, v6, v6 row_bcast:31 row_mask:0xc bank_mask:0xf
	v_add_f32_dpp v7, v7, v7 row_bcast:31 row_mask:0xc bank_mask:0xf
	v_add_f32_dpp v0, v0, v0 row_bcast:31 row_mask:0xc bank_mask:0xf
	v_add_f32_dpp v1, v1, v1 row_bcast:31 row_mask:0xc bank_mask:0xf
	v_add_f32_dpp v2, v2, v2 row_bcast:31 row_mask:0xc bank_mask:0xf
	v_add_f32_dpp v3, v3, v3 row_bcast:31 row_mask:0xc bank_mask:0xf
	v_mov_b32_e32 v37, v31
	v_mov_b32_e32 v35, v32
	v_mov_b32_e32 v38, v33
	v_mov_b32_e32 v36, v24
	v_mov_b32_e32 v39, v25
	v_mov_b32_e32 v40, v26
	v_mov_b32_e32 v41, v27
	v_mov_b32_e32 v42, v20
	v_mov_b32_e32 v43, v21
	v_mov_b32_e32 v46, v22
	v_mov_b32_e32 v48, v23
	v_mov_b32_e32 v47, v16
	v_mov_b32_e32 v49, v17
	v_mov_b32_e32 v52, v18
	v_mov_b32_e32 v53, v19
	v_mov_b32_e32 v50, v12
	v_mov_b32_e32 v51, v13
	v_mov_b32_e32 v54, v14
	v_mov_b32_e32 v56, v15
	v_mov_b32_e32 v55, v8
	v_mov_b32_e32 v57, v9
	v_mov_b32_e32 v60, v10
	v_mov_b32_e32 v61, v11
	v_mov_b32_e32 v58, v4
	v_mov_b32_e32 v59, v5
	v_mov_b32_e32 v62, v6
	v_mov_b32_e32 v65, v7
	v_mov_b32_e32 v63, v0
	v_mov_b32_e32 v66, v1
	v_mov_b32_e32 v64, v2
	v_mov_b32_e32 v67, v3
	s_nop 0
	v_add_u32_e32 v154, 0x3000, v149
	s_add_i32 s16, s16, s18
	v_mul_f32_e32 v30, 0x3fb8aa3b, v30
	v_exp_f32_e32 v30, v30
	s_waitcnt lgkmcnt(0)
	v_rcp_f32_e32 v44, v30
	s_waitcnt lgkmcnt(0)
	s_nop 0
	s_waitcnt lgkmcnt(0)
	s_nop 0
	s_waitcnt lgkmcnt(0)
	v_mul_f32_e32 v36, 0x3fb8aa3b, v36
	v_exp_f32_e32 v36, v36
	s_waitcnt lgkmcnt(0)
	s_nop 0
	s_waitcnt lgkmcnt(0)
	s_nop 0
	s_waitcnt lgkmcnt(0)
	s_nop 0
	s_waitcnt lgkmcnt(0)
	v_mul_f32_e32 v42, 0x3fb8aa3b, v42
	v_exp_f32_e32 v42, v42
	s_waitcnt lgkmcnt(0)
	v_mul_f32_e32 v43, 0x3fb8aa3b, v43
	v_exp_f32_e32 v43, v43
	s_waitcnt lgkmcnt(0)
	s_nop 0
	s_waitcnt lgkmcnt(0)
	s_nop 0
	s_waitcnt lgkmcnt(0)
	s_nop 0
	s_waitcnt lgkmcnt(0)
	s_nop 0
	s_waitcnt lgkmcnt(0)
	s_nop 0
	s_waitcnt lgkmcnt(0)
	s_nop 0
	s_waitcnt lgkmcnt(0)
	v_mul_f32_e32 v50, 0x3fb8aa3b, v50
	v_exp_f32_e32 v50, v50
	s_waitcnt lgkmcnt(0)
	v_mul_f32_e32 v51, 0x3fb8aa3b, v51
	v_exp_f32_e32 v51, v51
	s_waitcnt lgkmcnt(0)
	s_nop 0
	s_waitcnt lgkmcnt(0)
	s_nop 0
	s_waitcnt lgkmcnt(0)
	s_nop 0
	s_waitcnt lgkmcnt(0)
	s_nop 0
	s_waitcnt lgkmcnt(0)
	s_nop 0
	s_waitcnt lgkmcnt(0)
	s_nop 0
	s_waitcnt lgkmcnt(0)
	v_mul_f32_e32 v58, 0x3fb8aa3b, v58
	v_exp_f32_e32 v58, v58
	s_waitcnt lgkmcnt(0)
	v_lshl_add_u64 v[24:25], s[10:11], 0, v[28:29]
	v_mul_f32_e32 v59, 0x3fb8aa3b, v59
	v_exp_f32_e32 v59, v59
	v_lshl_add_u64 v[28:29], s[8:9], 0, v[28:29]
	s_waitcnt lgkmcnt(0)
	s_nop 0
	s_waitcnt lgkmcnt(0)
	s_nop 0
	s_waitcnt lgkmcnt(0)
	s_nop 0
	s_waitcnt lgkmcnt(0)
	v_mul_f32_e32 v31, 0x3fb8aa3b, v37
	v_exp_f32_e32 v31, v31
	v_mul_f32_e32 v37, 0x3fb8aa3b, v39
	v_exp_f32_e32 v37, v37
	s_waitcnt lgkmcnt(0)
	v_rcp_f32_e32 v45, v31
	v_pk_mul_f32 v[72:73], v[30:31], s[22:23] op_sel_hi:[1,0]
	s_waitcnt lgkmcnt(0)
	global_load_dwordx4 v[4:7], v[24:25], off offset:48
	global_load_dwordx4 v[12:15], v[24:25], off offset:32
	global_load_dwordx4 v[20:23], v[24:25], off offset:16
	global_load_dwordx4 v[68:71], v[24:25], off
	global_load_dwordx4 v[0:3], v[24:25], off offset:304
	global_load_dwordx4 v[8:11], v[24:25], off offset:288
	global_load_dwordx4 v[16:19], v[24:25], off offset:272
	s_nop 0
	global_load_dwordx4 v[24:27], v[24:25], off offset:256
	s_waitcnt vmcnt(4)
	v_lshlrev_b32_e32 v32, 16, v68
	v_and_b32_e32 v33, 0xffff0000, v68
	v_lshlrev_b32_e32 v34, 16, v69
	v_pk_mul_f32 v[32:33], v[72:73], v[32:33]
	s_waitcnt vmcnt(0)
	v_lshlrev_b32_e32 v30, 16, v24
	v_and_b32_e32 v31, 0xffff0000, v24
	v_mul_f32_e32 v24, 0x3fb8aa3b, v35
	v_pk_mul_f32 v[30:31], v[44:45], v[30:31]
	v_exp_f32_e32 v44, v24
	v_mul_f32_e32 v24, 0x3fb8aa3b, v38
	v_exp_f32_e32 v45, v24
	v_and_b32_e32 v35, 0xffff0000, v69
	v_rcp_f32_e32 v68, v44
	v_lshlrev_b32_e32 v24, 16, v25
	v_rcp_f32_e32 v69, v45
	v_pk_mul_f32 v[72:73], v[44:45], s[22:23] op_sel_hi:[1,0]
	v_rcp_f32_e32 v44, v36
	v_rcp_f32_e32 v45, v37
	v_and_b32_e32 v25, 0xffff0000, v25
	v_pk_mul_f32 v[24:25], v[68:69], v[24:25]
	v_pk_mul_f32 v[68:69], v[36:37], s[22:23] op_sel_hi:[1,0]
	v_lshlrev_b32_e32 v36, 16, v26
	v_and_b32_e32 v37, 0xffff0000, v26
	v_mul_f32_e32 v26, 0x3fb8aa3b, v40
	v_pk_mul_f32 v[36:37], v[44:45], v[36:37]
	v_exp_f32_e32 v44, v26
	v_mul_f32_e32 v26, 0x3fb8aa3b, v41
	v_exp_f32_e32 v45, v26
	v_lshlrev_b32_e32 v38, 16, v70
	v_and_b32_e32 v39, 0xffff0000, v70
	v_pk_mul_f32 v[38:39], v[68:69], v[38:39]
	v_rcp_f32_e32 v68, v44
	v_rcp_f32_e32 v69, v45
	v_lshlrev_b32_e32 v26, 16, v27
	v_and_b32_e32 v27, 0xffff0000, v27
	v_lshlrev_b32_e32 v40, 16, v71
	v_pk_mul_f32 v[26:27], v[68:69], v[26:27]
	v_rcp_f32_e32 v68, v42
	v_rcp_f32_e32 v69, v43
	v_and_b32_e32 v41, 0xffff0000, v71
	v_pk_mul_f32 v[70:71], v[44:45], s[22:23] op_sel_hi:[1,0]
	v_lshlrev_b32_e32 v44, 16, v20
	v_pk_mul_f32 v[40:41], v[70:71], v[40:41]
	v_pk_mul_f32 v[70:71], v[42:43], s[22:23] op_sel_hi:[1,0]
	v_lshlrev_b32_e32 v42, 16, v16
	v_and_b32_e32 v43, 0xffff0000, v16
	v_mul_f32_e32 v16, 0x3fb8aa3b, v46
	v_pk_mul_f32 v[42:43], v[68:69], v[42:43]
	v_exp_f32_e32 v68, v16
	v_mul_f32_e32 v16, 0x3fb8aa3b, v48
	v_exp_f32_e32 v69, v16
	v_and_b32_e32 v45, 0xffff0000, v20
	v_mul_f32_e32 v46, 0x3fb8aa3b, v47
	v_mul_f32_e32 v47, 0x3fb8aa3b, v49
	v_pk_mul_f32 v[44:45], v[70:71], v[44:45]
	v_rcp_f32_e32 v70, v68
	v_rcp_f32_e32 v71, v69
	v_exp_f32_e32 v46, v46
	v_exp_f32_e32 v47, v47
	v_lshlrev_b32_e32 v16, 16, v17
	v_and_b32_e32 v17, 0xffff0000, v17
	v_pk_mul_f32 v[34:35], v[72:73], v[34:35]
	v_pk_mul_f32 v[72:73], v[68:69], s[22:23] op_sel_hi:[1,0]
	v_pk_mul_f32 v[16:17], v[70:71], v[16:17]
	v_rcp_f32_e32 v68, v46
	v_pk_mul_f32 v[70:71], v[46:47], s[22:23] op_sel_hi:[1,0]
	v_rcp_f32_e32 v69, v47
	v_lshlrev_b32_e32 v46, 16, v18
	v_and_b32_e32 v47, 0xffff0000, v18
	v_mul_f32_e32 v18, 0x3fb8aa3b, v52
	v_exp_f32_e32 v52, v18
	v_mul_f32_e32 v18, 0x3fb8aa3b, v53
	v_exp_f32_e32 v53, v18
	v_pk_mul_f32 v[46:47], v[68:69], v[46:47]
	v_rcp_f32_e32 v68, v52
	v_lshlrev_b32_e32 v18, 16, v19
	v_rcp_f32_e32 v69, v53
	v_and_b32_e32 v19, 0xffff0000, v19
	v_lshlrev_b32_e32 v48, 16, v22
	v_and_b32_e32 v49, 0xffff0000, v22
	v_pk_mul_f32 v[18:19], v[68:69], v[18:19]
	v_rcp_f32_e32 v68, v50
	v_rcp_f32_e32 v69, v51
	v_pk_mul_f32 v[48:49], v[70:71], v[48:49]
	v_lshlrev_b32_e32 v22, 16, v23
	v_and_b32_e32 v23, 0xffff0000, v23
	v_pk_mul_f32 v[70:71], v[52:53], s[22:23] op_sel_hi:[1,0]
	v_lshlrev_b32_e32 v52, 16, v12
	v_pk_mul_f32 v[22:23], v[70:71], v[22:23]
	v_pk_mul_f32 v[70:71], v[50:51], s[22:23] op_sel_hi:[1,0]
	v_lshlrev_b32_e32 v50, 16, v8
	v_and_b32_e32 v51, 0xffff0000, v8
	v_mul_f32_e32 v8, 0x3fb8aa3b, v54
	v_pk_mul_f32 v[50:51], v[68:69], v[50:51]
	v_exp_f32_e32 v68, v8
	v_mul_f32_e32 v8, 0x3fb8aa3b, v56
	v_exp_f32_e32 v69, v8
	v_and_b32_e32 v53, 0xffff0000, v12
	v_mul_f32_e32 v54, 0x3fb8aa3b, v55
	v_mul_f32_e32 v55, 0x3fb8aa3b, v57
	v_pk_mul_f32 v[52:53], v[70:71], v[52:53]
	v_rcp_f32_e32 v70, v68
	v_rcp_f32_e32 v71, v69
	v_exp_f32_e32 v54, v54
	v_exp_f32_e32 v55, v55
	v_lshlrev_b32_e32 v20, 16, v21
	v_and_b32_e32 v21, 0xffff0000, v21
	v_lshlrev_b32_e32 v8, 16, v9
	v_and_b32_e32 v9, 0xffff0000, v9
	v_pk_mul_f32 v[20:21], v[72:73], v[20:21]
	v_pk_mul_f32 v[72:73], v[68:69], s[22:23] op_sel_hi:[1,0]
	v_pk_mul_f32 v[8:9], v[70:71], v[8:9]
	v_rcp_f32_e32 v68, v54
	v_pk_mul_f32 v[70:71], v[54:55], s[22:23] op_sel_hi:[1,0]
	v_rcp_f32_e32 v69, v55
	v_lshlrev_b32_e32 v54, 16, v10
	v_and_b32_e32 v55, 0xffff0000, v10
	v_mul_f32_e32 v10, 0x3fb8aa3b, v60
	v_exp_f32_e32 v60, v10
	v_mul_f32_e32 v10, 0x3fb8aa3b, v61
	v_exp_f32_e32 v61, v10
	v_pk_mul_f32 v[54:55], v[68:69], v[54:55]
	v_rcp_f32_e32 v68, v60
	v_lshlrev_b32_e32 v10, 16, v11
	v_rcp_f32_e32 v69, v61
	v_and_b32_e32 v11, 0xffff0000, v11
	v_lshlrev_b32_e32 v56, 16, v14
	v_and_b32_e32 v57, 0xffff0000, v14
	v_pk_mul_f32 v[10:11], v[68:69], v[10:11]
	v_rcp_f32_e32 v68, v58
	v_rcp_f32_e32 v69, v59
	v_pk_mul_f32 v[56:57], v[70:71], v[56:57]
	v_lshlrev_b32_e32 v14, 16, v15
	v_and_b32_e32 v15, 0xffff0000, v15
	v_pk_mul_f32 v[70:71], v[60:61], s[22:23] op_sel_hi:[1,0]
	v_lshlrev_b32_e32 v60, 16, v4
	v_pk_mul_f32 v[14:15], v[70:71], v[14:15]
	v_pk_mul_f32 v[70:71], v[58:59], s[22:23] op_sel_hi:[1,0]
	v_lshlrev_b32_e32 v58, 16, v0
	v_and_b32_e32 v59, 0xffff0000, v0
	v_mul_f32_e32 v0, 0x3fb8aa3b, v62
	v_pk_mul_f32 v[58:59], v[68:69], v[58:59]
	v_exp_f32_e32 v68, v0
	v_mul_f32_e32 v0, 0x3fb8aa3b, v65
	v_exp_f32_e32 v69, v0
	v_and_b32_e32 v61, 0xffff0000, v4
	v_pk_mul_f32 v[60:61], v[70:71], v[60:61]
	v_rcp_f32_e32 v4, v68
	v_lshlrev_b32_e32 v70, 16, v5
	v_and_b32_e32 v71, 0xffff0000, v5
	v_rcp_f32_e32 v5, v69
	v_lshlrev_b32_e32 v0, 16, v1
	v_and_b32_e32 v1, 0xffff0000, v1
	v_lshlrev_b32_e32 v12, 16, v13
	v_pk_mul_f32 v[4:5], v[4:5], v[0:1]
	v_mul_f32_e32 v0, 0x3fb8aa3b, v63
	v_mul_f32_e32 v1, 0x3fb8aa3b, v66
	v_exp_f32_e32 v0, v0
	v_exp_f32_e32 v1, v1
	v_and_b32_e32 v13, 0xffff0000, v13
	v_pk_mul_f32 v[12:13], v[72:73], v[12:13]
	v_rcp_f32_e32 v62, v0
	v_rcp_f32_e32 v63, v1
	v_pk_mul_f32 v[72:73], v[68:69], s[22:23] op_sel_hi:[1,0]
	v_lshlrev_b32_e32 v68, 16, v6
	v_pk_mul_f32 v[70:71], v[72:73], v[70:71]
	v_pk_mul_f32 v[72:73], v[0:1], s[22:23] op_sel_hi:[1,0]
	v_lshlrev_b32_e32 v0, 16, v2
	v_and_b32_e32 v1, 0xffff0000, v2
	v_pk_mul_f32 v[62:63], v[62:63], v[0:1]
	v_mul_f32_e32 v0, 0x3fb8aa3b, v64
	v_mul_f32_e32 v1, 0x3fb8aa3b, v67
	v_exp_f32_e32 v0, v0
	v_exp_f32_e32 v1, v1
	v_and_b32_e32 v69, 0xffff0000, v6
	v_lshlrev_b32_e32 v64, 16, v7
	v_rcp_f32_e32 v6, v0
	v_and_b32_e32 v65, 0xffff0000, v7
	v_rcp_f32_e32 v7, v1
	v_pk_mul_f32 v[66:67], v[0:1], s[22:23] op_sel_hi:[1,0]
	v_lshlrev_b32_e32 v0, 16, v3
	v_and_b32_e32 v1, 0xffff0000, v3
	v_pk_mul_f32 v[6:7], v[6:7], v[0:1]
	v_cvt_pk_bf16_f32 v0, v32, v33
	v_cvt_pk_bf16_f32 v1, v34, v35
	v_cvt_pk_bf16_f32 v2, v38, v39
	v_cvt_pk_bf16_f32 v3, v40, v41
	ds_write_b128 v99, v[0:3]
	v_cvt_pk_bf16_f32 v0, v30, v31
	v_cvt_pk_bf16_f32 v1, v24, v25
	v_cvt_pk_bf16_f32 v2, v36, v37
	v_cvt_pk_bf16_f32 v3, v26, v27
	ds_write_b128 v99, v[0:3] offset:4096
	v_cvt_pk_bf16_f32 v0, v44, v45
	v_cvt_pk_bf16_f32 v1, v20, v21
	v_cvt_pk_bf16_f32 v2, v48, v49
	v_cvt_pk_bf16_f32 v3, v22, v23
	ds_write_b128 v99, v[0:3] offset:16
	v_cvt_pk_bf16_f32 v0, v42, v43
	v_cvt_pk_bf16_f32 v1, v16, v17
	v_cvt_pk_bf16_f32 v2, v46, v47
	v_cvt_pk_bf16_f32 v3, v18, v19
	ds_write_b128 v99, v[0:3] offset:4112
	v_cvt_pk_bf16_f32 v0, v52, v53
	v_cvt_pk_bf16_f32 v1, v12, v13
	v_cvt_pk_bf16_f32 v2, v56, v57
	v_cvt_pk_bf16_f32 v3, v14, v15
	v_pk_mul_f32 v[68:69], v[72:73], v[68:69]
	v_pk_mul_f32 v[64:65], v[66:67], v[64:65]
	ds_write_b128 v99, v[0:3] offset:32
	v_cvt_pk_bf16_f32 v0, v50, v51
	v_cvt_pk_bf16_f32 v1, v8, v9
	v_cvt_pk_bf16_f32 v2, v54, v55
	v_cvt_pk_bf16_f32 v3, v10, v11
	ds_write_b128 v99, v[0:3] offset:4128
	v_cvt_pk_bf16_f32 v0, v60, v61
	v_cvt_pk_bf16_f32 v1, v70, v71
	v_cvt_pk_bf16_f32 v2, v68, v69
	v_cvt_pk_bf16_f32 v3, v64, v65
	ds_write_b128 v99, v[0:3] offset:48
	v_cvt_pk_bf16_f32 v0, v58, v59
	v_cvt_pk_bf16_f32 v1, v4, v5
	v_cvt_pk_bf16_f32 v2, v62, v63
	v_cvt_pk_bf16_f32 v3, v6, v7
	ds_write_b128 v99, v[0:3] offset:4144
	global_load_dwordx4 v[0:3], v[28:29], off offset:48
	global_load_dwordx4 v[4:7], v[28:29], off offset:32
	global_load_dwordx4 v[8:11], v[28:29], off offset:16
	global_load_dwordx4 v[12:15], v[28:29], off
	global_load_dwordx4 v[16:19], v[28:29], off offset:112
	global_load_dwordx4 v[20:23], v[28:29], off offset:96
	global_load_dwordx4 v[24:27], v[28:29], off offset:80
	s_nop 0
	global_load_dwordx4 v[28:31], v[28:29], off offset:64
	s_waitcnt vmcnt(0)
	ds_write_b16 v103, v12 offset:8192
	ds_write_b16_d16_hi v103, v12 offset:8320
	ds_write_b16 v103, v13 offset:8448
	ds_write_b16_d16_hi v103, v13 offset:8576
	ds_write_b16 v103, v14 offset:8704
	ds_write_b16_d16_hi v103, v14 offset:8832
	ds_write_b16 v103, v15 offset:8960
	ds_write_b16_d16_hi v103, v15 offset:9088
	ds_write_b16 v103, v8 offset:9216
	ds_write_b16_d16_hi v103, v8 offset:9344
	ds_write_b16 v103, v9 offset:9472
	ds_write_b16_d16_hi v103, v9 offset:9600
	ds_write_b16 v103, v10 offset:9728
	ds_write_b16_d16_hi v103, v10 offset:9856
	ds_write_b16 v103, v11 offset:9984
	ds_write_b16_d16_hi v103, v11 offset:10112
	ds_write_b16 v103, v4 offset:10240
	ds_write_b16_d16_hi v103, v4 offset:10368
	ds_write_b16 v103, v5 offset:10496
	ds_write_b16_d16_hi v103, v5 offset:10624
	ds_write_b16 v103, v6 offset:10752
	ds_write_b16_d16_hi v103, v6 offset:10880
	ds_write_b16 v103, v7 offset:11008
	ds_write_b16_d16_hi v103, v7 offset:11136
	ds_write_b16 v103, v0 offset:11264
	ds_write_b16_d16_hi v103, v0 offset:11392
	ds_write_b16 v103, v1 offset:11520
	ds_write_b16_d16_hi v103, v1 offset:11648
	ds_write_b16 v103, v2 offset:11776
	ds_write_b16_d16_hi v103, v2 offset:11904
	ds_write_b16 v103, v3 offset:12032
	ds_write_b16_d16_hi v103, v3 offset:12160
	ds_write_b16 v103, v28 offset:12288
	ds_write_b16_d16_hi v103, v28 offset:12416
	ds_write_b16 v103, v29 offset:12544
	ds_write_b16_d16_hi v103, v29 offset:12672
	ds_write_b16 v103, v30 offset:12800
	ds_write_b16_d16_hi v103, v30 offset:12928
	ds_write_b16 v103, v31 offset:13056
	ds_write_b16_d16_hi v103, v31 offset:13184
	ds_write_b16 v103, v24 offset:13312
	ds_write_b16_d16_hi v103, v24 offset:13440
	ds_write_b16 v103, v25 offset:13568
	ds_write_b16_d16_hi v103, v25 offset:13696
	ds_write_b16 v103, v26 offset:13824
	ds_write_b16_d16_hi v103, v26 offset:13952
	ds_write_b16 v103, v27 offset:14080
	ds_write_b16_d16_hi v103, v27 offset:14208
	ds_write_b16 v103, v20 offset:14336
	ds_write_b16_d16_hi v103, v20 offset:14464
	ds_write_b16 v103, v21 offset:14592
	ds_write_b16_d16_hi v103, v21 offset:14720
	ds_write_b16 v103, v22 offset:14848
	ds_write_b16_d16_hi v103, v22 offset:14976
	ds_write_b16 v103, v23 offset:15104
	ds_write_b16_d16_hi v103, v23 offset:15232
	ds_write_b16 v103, v16 offset:15360
	ds_write_b16_d16_hi v103, v16 offset:15488
	ds_write_b16 v103, v17 offset:15616
	ds_write_b16_d16_hi v103, v17 offset:15744
	ds_write_b16 v103, v18 offset:15872
	ds_write_b16_d16_hi v103, v18 offset:16000
	ds_write_b16 v103, v19 offset:16128
	ds_write_b16_d16_hi v103, v19 offset:16256
	s_waitcnt lgkmcnt(0)
	ds_read_b128 v[0:3], v148 offset:4096
	ds_read_b128 v[72:75], v148
	ds_read_b128 v[64:67], v148 offset:32
	ds_read_b128 v[48:51], v148 offset:4128
	ds_read_b128 v[76:79], v148 offset:2048
	ds_read_b128 v[32:35], v148 offset:6144
	ds_read_b128 v[68:71], v148 offset:2080
	ds_read_b128 v[52:55], v148 offset:6176
	s_waitcnt lgkmcnt(6)
	v_mfma_f32_32x32x16_bf16 v[16:31], v[0:3], v[72:75], 0
	s_waitcnt lgkmcnt(3)
	v_mfma_f32_32x32x16_bf16 v[0:15], v[0:3], v[76:79], 0
	s_waitcnt lgkmcnt(1)
	v_mfma_f32_32x32x16_bf16 v[0:15], v[48:51], v[68:71], v[0:15]
	v_mfma_f32_32x32x16_bf16 v[32:47], v[32:35], v[76:79], 0
	s_nop 10
	v_cvt_pk_bf16_f32 v86, v12, v13
	v_add_u32_e32 v12, 0x2000, v149
	v_cvt_pk_bf16_f32 v0, v0, v1
	v_cvt_pk_bf16_f32 v1, v2, v3
	v_cvt_pk_bf16_f32 v2, v4, v5
	v_cvt_pk_bf16_f32 v3, v6, v7
	v_cvt_pk_bf16_f32 v84, v8, v9
	v_mfma_f32_32x32x16_bf16 v[16:31], v[48:51], v[64:67], v[16:31]
	v_cvt_pk_bf16_f32 v85, v10, v11
	ds_read2_b64 v[4:7], v12 offset1:2
	ds_read2_b64 v[8:11], v12 offset0:4 offset1:6
	v_cvt_pk_bf16_f32 v87, v14, v15
	s_waitcnt lgkmcnt(2)
	v_mfma_f32_32x32x16_bf16 v[32:47], v[52:55], v[68:71], v[32:47]
	s_nop 5
	v_cndmask_b32_e64 v16, v16, 0, s[48:49]
	v_cndmask_b32_e64 v17, 0, v17, s[50:51]
	v_cndmask_b32_e64 v18, v18, 0, s[52:53]
	v_cndmask_b32_e64 v19, v19, 0, s[54:55]
	v_cndmask_b32_e64 v20, v20, 0, s[56:57]
	v_cndmask_b32_e64 v21, v21, 0, s[58:59]
	v_cndmask_b32_e64 v22, v22, 0, s[60:61]
	v_cndmask_b32_e64 v23, v23, 0, s[62:63]
	v_cndmask_b32_e64 v24, v24, 0, s[64:65]
	v_cndmask_b32_e64 v25, v25, 0, s[66:67]
	v_cndmask_b32_e64 v26, v26, 0, s[68:69]
	v_cndmask_b32_e64 v27, v27, 0, s[70:71]
	v_cndmask_b32_e64 v28, v28, 0, s[72:73]
	v_cndmask_b32_e64 v29, v29, 0, s[74:75]
	v_cndmask_b32_e64 v30, v30, 0, s[76:77]
	v_cndmask_b32_e64 v31, v31, 0, s[78:79]
	v_cvt_pk_bf16_f32 v48, v16, v17
	v_cvt_pk_bf16_f32 v49, v18, v19
	v_cvt_pk_bf16_f32 v50, v20, v21
	v_cvt_pk_bf16_f32 v51, v22, v23
	v_cvt_pk_bf16_f32 v80, v24, v25
	v_cvt_pk_bf16_f32 v81, v26, v27
	v_cvt_pk_bf16_f32 v82, v28, v29
	v_cvt_pk_bf16_f32 v83, v30, v31
	s_waitcnt lgkmcnt(1)
	v_mfma_f32_32x32x16_bf16 v[16:31], v[4:7], v[0:3], 0
	v_cndmask_b32_e64 v32, v32, 0, s[48:49]
	v_cndmask_b32_e64 v33, 0, v33, s[50:51]
	v_cndmask_b32_e64 v34, v34, 0, s[52:53]
	v_cndmask_b32_e64 v35, v35, 0, s[54:55]
	v_cndmask_b32_e64 v36, v36, 0, s[56:57]
	v_cndmask_b32_e64 v37, v37, 0, s[58:59]
	v_cndmask_b32_e64 v38, v38, 0, s[60:61]
	v_cndmask_b32_e64 v39, v39, 0, s[62:63]
	v_cndmask_b32_e64 v40, v40, 0, s[64:65]
	v_cndmask_b32_e64 v41, v41, 0, s[66:67]
	v_cndmask_b32_e64 v42, v42, 0, s[68:69]
	v_cndmask_b32_e64 v43, v43, 0, s[70:71]
	v_cndmask_b32_e64 v44, v44, 0, s[72:73]
	v_cndmask_b32_e64 v45, v45, 0, s[74:75]
	v_cndmask_b32_e64 v46, v46, 0, s[76:77]
	v_cndmask_b32_e64 v47, v47, 0, s[78:79]
	v_cvt_pk_bf16_f32 v88, v32, v33
	v_cvt_pk_bf16_f32 v89, v34, v35
	v_cvt_pk_bf16_f32 v90, v36, v37
	v_cvt_pk_bf16_f32 v91, v38, v39
	v_cvt_pk_bf16_f32 v92, v40, v41
	v_cvt_pk_bf16_f32 v93, v42, v43
	v_cvt_pk_bf16_f32 v94, v44, v45
	v_cvt_pk_bf16_f32 v95, v46, v47
	v_mfma_f32_32x32x16_bf16 v[32:47], v[4:7], v[48:51], 0
	ds_read2_b64 v[4:7], v12 offset0:8 offset1:10
	s_waitcnt lgkmcnt(1)
	v_mfma_f32_32x32x16_bf16 v[16:31], v[8:11], v[84:87], v[16:31]
	s_waitcnt lgkmcnt(0)
	v_mfma_f32_32x32x16_bf16 v[16:31], v[4:7], v[88:91], v[16:31]
	ds_read2_b64 v[4:7], v12 offset0:12 offset1:14
	s_waitcnt lgkmcnt(0)
	v_mfma_f32_32x32x16_bf16 v[16:31], v[4:7], v[92:95], v[16:31]
	v_lshl_add_u64 v[4:5], s[12:13], 0, v[136:137]
	global_load_dword v6, v[4:5], off
	v_lshl_add_u64 v[4:5], s[12:13], 0, v[128:129]
	v_mfma_f32_32x32x16_bf16 v[32:47], v[8:11], v[80:83], v[32:47]
	global_load_dword v7, v[4:5], off offset:-768
	global_load_dword v8, v[4:5], off offset:-512
	global_load_dword v9, v[4:5], off offset:-256
	global_load_dword v10, v[4:5], off
	global_load_dword v11, v[4:5], off offset:256
	global_load_dword v12, v[4:5], off offset:512
	global_load_dword v13, v[4:5], off offset:768
	ds_read2_b64 v[150:153], v154 offset0:4 offset1:6
	s_waitcnt vmcnt(6)
	v_cvt_pk_bf16_f32 v4, v6, v7
	s_waitcnt vmcnt(4)
	v_cvt_pk_bf16_f32 v5, v8, v9
	s_waitcnt vmcnt(2)
	v_cvt_pk_bf16_f32 v6, v10, v11
	s_waitcnt vmcnt(0)
	v_cvt_pk_bf16_f32 v7, v12, v13
	s_nop 1
	v_mfma_f32_32x32x16_bf16 v[32:47], v[4:7], v[72:75], v[32:47]
	v_mfma_f32_32x32x16_bf16 v[16:31], v[4:7], v[76:79], v[16:31]
	v_lshl_add_u64 v[4:5], s[12:13], 0, v[138:139]
	global_load_dword v6, v[4:5], off
	v_lshl_add_u64 v[4:5], s[12:13], 0, v[140:141]
	global_load_dword v7, v[4:5], off
	v_lshl_add_u64 v[4:5], s[12:13], 0, v[142:143]
	global_load_dword v8, v[4:5], off
	v_lshl_add_u64 v[4:5], s[12:13], 0, v[144:145]
	global_load_dword v9, v[4:5], off
	v_lshl_add_u64 v[4:5], s[12:13], 0, v[146:147]
	global_load_dword v10, v[4:5], off
	v_lshl_add_u64 v[4:5], s[12:13], 0, v[134:135]
	global_load_dword v11, v[4:5], off
	v_lshl_add_u64 v[4:5], s[12:13], 0, v[132:133]
	global_load_dword v12, v[4:5], off
	v_lshl_add_u64 v[4:5], s[12:13], 0, v[130:131]
	global_load_dword v13, v[4:5], off
	s_waitcnt vmcnt(6)
	v_cvt_pk_bf16_f32 v4, v6, v7
	s_waitcnt vmcnt(4)
	v_cvt_pk_bf16_f32 v5, v8, v9
	s_waitcnt vmcnt(2)
	v_cvt_pk_bf16_f32 v6, v10, v11
	s_waitcnt vmcnt(0)
	v_cvt_pk_bf16_f32 v7, v12, v13
	s_nop 1
	v_mfma_f32_32x32x16_bf16 v[32:47], v[4:7], v[64:67], v[32:47]
	v_mfma_f32_32x32x16_bf16 v[16:31], v[4:7], v[68:71], v[16:31]
	ds_read2_b64 v[4:7], v154 offset1:2
	s_waitcnt lgkmcnt(0)
	v_mfma_f32_32x32x16_bf16 v[48:63], v[4:7], v[48:51], 0
	v_mfma_f32_32x32x16_bf16 v[0:15], v[4:7], v[0:3], 0
	v_mfma_f32_32x32x16_bf16 v[48:63], v[150:153], v[80:83], v[48:63]
	ds_read2_b64 v[80:83], v154 offset0:8 offset1:10
	v_mfma_f32_32x32x16_bf16 v[0:15], v[150:153], v[84:87], v[0:15]
	s_waitcnt lgkmcnt(0)
	v_mfma_f32_32x32x16_bf16 v[0:15], v[80:83], v[88:91], v[0:15]
	ds_read2_b64 v[80:83], v154 offset0:12 offset1:14
	s_waitcnt lgkmcnt(0)
	v_mfma_f32_32x32x16_bf16 v[0:15], v[80:83], v[92:95], v[0:15]
	v_lshl_add_u64 v[80:81], s[12:13], 0, v[126:127]
	global_load_dword v82, v[80:81], off
	v_lshl_add_u64 v[80:81], s[12:13], 0, v[114:115]
	global_load_dword v83, v[80:81], off offset:-768
	global_load_dword v84, v[80:81], off offset:-512
	global_load_dword v85, v[80:81], off offset:-256
	global_load_dword v86, v[80:81], off
	global_load_dword v87, v[80:81], off offset:256
	global_load_dword v88, v[80:81], off offset:512
	global_load_dword v89, v[80:81], off offset:768
	s_waitcnt vmcnt(4)
	v_cvt_pk_bf16_f32 v81, v84, v85
	v_cvt_pk_bf16_f32 v80, v82, v83
	s_waitcnt vmcnt(2)
	v_cvt_pk_bf16_f32 v82, v86, v87
	s_waitcnt vmcnt(0)
	v_cvt_pk_bf16_f32 v83, v88, v89
	s_nop 1
	v_mfma_f32_32x32x16_bf16 v[48:63], v[80:83], v[72:75], v[48:63]
	v_lshl_add_u64 v[72:73], s[12:13], 0, v[124:125]
	global_load_dword v74, v[72:73], off
	v_lshl_add_u64 v[72:73], s[12:13], 0, v[122:123]
	global_load_dword v75, v[72:73], off
	v_lshl_add_u64 v[72:73], s[12:13], 0, v[120:121]
	v_mfma_f32_32x32x16_bf16 v[0:15], v[80:83], v[76:79], v[0:15]
	global_load_dword v76, v[72:73], off
	v_lshl_add_u64 v[72:73], s[12:13], 0, v[118:119]
	global_load_dword v77, v[72:73], off
	v_lshl_add_u64 v[72:73], s[12:13], 0, v[116:117]
	global_load_dword v78, v[72:73], off
	v_lshl_add_u64 v[72:73], s[12:13], 0, v[112:113]
	global_load_dword v79, v[72:73], off
	v_lshl_add_u64 v[72:73], s[12:13], 0, v[110:111]
	global_load_dword v80, v[72:73], off
	v_lshl_add_u64 v[72:73], s[12:13], 0, v[96:97]
	global_load_dword v81, v[72:73], off
	s_add_u32 s12, s12, s20
	s_addc_u32 s13, s13, s21
	s_cmpk_gt_i32 s16, 0x3ff
	s_waitcnt vmcnt(6)
	v_cvt_pk_bf16_f32 v72, v74, v75
	s_waitcnt vmcnt(4)
	v_cvt_pk_bf16_f32 v73, v76, v77
	s_waitcnt vmcnt(2)
	v_cvt_pk_bf16_f32 v74, v78, v79
	s_waitcnt vmcnt(0)
	v_cvt_pk_bf16_f32 v75, v80, v81
	s_nop 1
	v_mfma_f32_32x32x16_bf16 v[48:63], v[72:75], v[64:67], v[48:63]
	v_mul_f32_e32 v66, v33, v33
	v_fmac_f32_e32 v66, v32, v32
	v_fmac_f32_e32 v66, v34, v34
	v_fmac_f32_e32 v66, v35, v35
	v_fmac_f32_e32 v66, v36, v36
	v_fmac_f32_e32 v66, v37, v37
	v_fmac_f32_e32 v66, v38, v38
	v_fmac_f32_e32 v66, v39, v39
	v_fmac_f32_e32 v66, v40, v40
	v_fmac_f32_e32 v66, v41, v41
	v_fmac_f32_e32 v66, v42, v42
	v_fmac_f32_e32 v66, v43, v43
	v_fmac_f32_e32 v66, v44, v44
	v_fmac_f32_e32 v66, v45, v45
	v_fmac_f32_e32 v66, v46, v46
	v_fmac_f32_e32 v66, v47, v47
	v_fmac_f32_e32 v66, v48, v48
	v_fmac_f32_e32 v66, v49, v49
	v_fmac_f32_e32 v66, v50, v50
	v_fmac_f32_e32 v66, v51, v51
	v_fmac_f32_e32 v66, v52, v52
	v_fmac_f32_e32 v66, v53, v53
	v_fmac_f32_e32 v66, v54, v54
	v_fmac_f32_e32 v66, v55, v55
	v_fmac_f32_e32 v66, v56, v56
	v_fmac_f32_e32 v66, v57, v57
	v_fmac_f32_e32 v66, v58, v58
	v_fmac_f32_e32 v66, v59, v59
	v_fmac_f32_e32 v66, v60, v60
	v_fmac_f32_e32 v66, v61, v61
	v_pk_mul_f32 v[64:65], v[62:63], v[62:63]
	v_mfma_f32_32x32x16_bf16 v[0:15], v[72:75], v[68:71], v[0:15]
	v_add_f32_e32 v64, v64, v66
	v_add_f32_e32 v64, v65, v64
	v_mov_b32_e32 v65, v64
	s_nop 1
	v_permlane32_swap_b32_e32 v64, v65
	v_add_f32_e32 v64, v64, v65
	v_fmamk_f32 v64, v64, 0x3c800000, v241
	v_cmp_gt_f32_e32 vcc, s1, v64
	v_mul_f32_e32 v65, 0x4f800000, v64
	v_mov_b32_e32 v71, s15
	v_cndmask_b32_e32 v64, v64, v65, vcc
	v_sqrt_f32_e32 v65, v64
	v_or_b32_e32 v70, s14, v198
	v_add_u32_e32 v66, -1, v65
	v_fma_f32 v67, -v66, v65, v64
	v_cmp_ge_f32_e64 s[2:3], 0, v67
	v_add_u32_e32 v67, 1, v65
	s_nop 0
	v_cndmask_b32_e64 v66, v65, v66, s[2:3]
	v_fma_f32 v65, -v67, v65, v64
	v_cmp_lt_f32_e64 s[2:3], 0, v65
	s_nop 1
	v_cndmask_b32_e64 v65, v66, v67, s[2:3]
	v_mul_f32_e32 v66, 0x37800000, v65
	v_cndmask_b32_e32 v65, v65, v66, vcc
	v_cmp_class_f32_e32 vcc, v64, v240
	s_nop 1
	v_cndmask_b32_e32 v64, v65, v64, vcc
	v_div_scale_f32 v65, s[2:3], v64, v64, 1.0
	v_rcp_f32_e32 v66, v65
	s_nop 0
	v_fma_f32 v67, -v65, v66, 1.0
	v_fmac_f32_e32 v66, v67, v66
	v_div_scale_f32 v67, vcc, 1.0, v64, 1.0
	v_mul_f32_e32 v68, v67, v66
	v_fma_f32 v69, -v65, v68, v67
	v_fmac_f32_e32 v68, v69, v66
	v_fma_f32 v65, -v65, v68, v67
	v_div_fmas_f32 v65, v65, v66, v68
	v_lshlrev_b64 v[66:67], 9, v[70:71]
	v_lshl_add_u64 v[72:73], v[106:107], 0, v[66:67]
	global_load_dwordx2 v[74:75], v[72:73], off
	global_load_dwordx4 v[66:69], v[104:105], off
	v_div_fixup_f32 v64, v65, v64, 1.0
	s_waitcnt vmcnt(1)
	v_lshlrev_b32_e32 v76, 16, v74
	v_mul_f32_e32 v65, 0xbfb8aa3b, v76
	v_exp_f32_e32 v65, v65
	v_and_b32_e32 v77, 0xffff0000, v74
	v_add_f32_e32 v65, 1.0, v65
	v_rcp_f32_e32 v78, v65
	v_pk_mul_f32 v[32:33], v[32:33], v[64:65] op_sel_hi:[1,0]
	v_mul_f32_e32 v65, 0xbfb8aa3b, v77
	v_exp_f32_e32 v65, v65
	s_waitcnt vmcnt(0)
	v_pk_mul_f32 v[32:33], v[66:67], v[32:33]
	v_add_f32_e32 v65, 1.0, v65
	v_rcp_f32_e32 v79, v65
	s_nop 0
	v_pk_mul_f32 v[66:67], v[78:79], v[76:77]
	s_nop 0
	v_pk_mul_f32 v[32:33], v[32:33], v[66:67]
	v_lshlrev_b32_e32 v66, 16, v75
	v_mul_f32_e32 v65, 0xbfb8aa3b, v66
	v_exp_f32_e32 v65, v65
	v_and_b32_e32 v67, 0xffff0000, v75
	v_cvt_pk_bf16_f32 v32, v32, v33
	v_add_f32_e32 v65, 1.0, v65
	v_rcp_f32_e32 v74, v65
	v_pk_mul_f32 v[34:35], v[34:35], v[64:65] op_sel_hi:[1,0]
	v_mul_f32_e32 v65, 0xbfb8aa3b, v67
	v_exp_f32_e32 v65, v65
	v_pk_mul_f32 v[34:35], v[68:69], v[34:35]
	v_add_f32_e32 v65, 1.0, v65
	v_rcp_f32_e32 v75, v65
	s_nop 0
	v_pk_mul_f32 v[66:67], v[74:75], v[66:67]
	s_nop 0
	v_pk_mul_f32 v[34:35], v[34:35], v[66:67]
	v_mad_u64_u32 v[66:67], s[2:3], v70, s83, v[108:109]
	v_cvt_pk_bf16_f32 v33, v34, v35
	v_mad_i32_i24 v67, s15, v227, v67
	global_store_dwordx2 v[66:67], v[32:33], off
	global_load_dwordx2 v[68:69], v[72:73], off offset:16
	s_nop 0
	global_load_dwordx4 v[32:35], v[104:105], off offset:32
	s_waitcnt vmcnt(1)
	v_lshlrev_b32_e32 v70, 16, v68
	v_mul_f32_e32 v65, 0xbfb8aa3b, v70
	v_exp_f32_e32 v65, v65
	v_and_b32_e32 v71, 0xffff0000, v68
	v_add_f32_e32 v65, 1.0, v65
	v_pk_mul_f32 v[36:37], v[36:37], v[64:65] op_sel_hi:[1,0]
	v_rcp_f32_e32 v74, v65
	s_waitcnt vmcnt(0)
	v_pk_mul_f32 v[32:33], v[32:33], v[36:37]
	v_mul_f32_e32 v36, 0xbfb8aa3b, v71
	v_exp_f32_e32 v36, v36
	s_nop 0
	v_add_f32_e32 v36, 1.0, v36
	v_rcp_f32_e32 v75, v36
	s_nop 0
	v_pk_mul_f32 v[36:37], v[74:75], v[70:71]
	s_nop 0
	v_pk_mul_f32 v[32:33], v[32:33], v[36:37]
	v_lshlrev_b32_e32 v36, 16, v69
	v_mul_f32_e32 v65, 0xbfb8aa3b, v36
	v_exp_f32_e32 v65, v65
	v_and_b32_e32 v37, 0xffff0000, v69
	v_cvt_pk_bf16_f32 v32, v32, v33
	v_add_f32_e32 v65, 1.0, v65
	v_pk_mul_f32 v[38:39], v[38:39], v[64:65] op_sel_hi:[1,0]
	v_rcp_f32_e32 v68, v65
	v_pk_mul_f32 v[34:35], v[34:35], v[38:39]
	v_mul_f32_e32 v38, 0xbfb8aa3b, v37
	v_exp_f32_e32 v38, v38
	v_pk_mul_f32 v[40:41], v[40:41], v[64:65] op_sel_hi:[1,0]
	v_add_f32_e32 v38, 1.0, v38
	v_rcp_f32_e32 v69, v38
	s_nop 0
	v_pk_mul_f32 v[36:37], v[68:69], v[36:37]
	s_nop 0
	v_pk_mul_f32 v[34:35], v[34:35], v[36:37]
	s_nop 0
	v_cvt_pk_bf16_f32 v33, v34, v35
	global_store_dwordx2 v[66:67], v[32:33], off offset:16
	global_load_dwordx2 v[36:37], v[72:73], off offset:32
	s_nop 0
	global_load_dwordx4 v[32:35], v[104:105], off offset:64
	s_waitcnt vmcnt(1)
	v_lshlrev_b32_e32 v38, 16, v36
	v_and_b32_e32 v39, 0xffff0000, v36
	v_mul_f32_e32 v36, 0xbfb8aa3b, v38
	v_exp_f32_e32 v36, v36
	s_waitcnt vmcnt(0)
	v_pk_mul_f32 v[32:33], v[40:41], v[32:33]
	v_pk_mul_f32 v[40:41], v[42:43], v[64:65] op_sel_hi:[1,0]
	v_pk_mul_f32 v[42:43], v[44:45], v[64:65] op_sel_hi:[1,0]
	v_add_f32_e32 v36, 1.0, v36
	v_rcp_f32_e32 v68, v36
	v_mul_f32_e32 v36, 0xbfb8aa3b, v39
	v_exp_f32_e32 v36, v36
	v_pk_mul_f32 v[34:35], v[40:41], v[34:35]
	v_add_f32_e32 v36, 1.0, v36
	v_rcp_f32_e32 v69, v36
	v_lshlrev_b32_e32 v36, 16, v37
	v_and_b32_e32 v37, 0xffff0000, v37
	v_pk_mul_f32 v[38:39], v[68:69], v[38:39]
	s_nop 0
	v_pk_mul_f32 v[32:33], v[32:33], v[38:39]
	v_mul_f32_e32 v38, 0xbfb8aa3b, v36
	v_mul_f32_e32 v39, 0xbfb8aa3b, v37
	v_exp_f32_e32 v38, v38
	v_exp_f32_e32 v39, v39
	v_cvt_pk_bf16_f32 v32, v32, v33
	v_add_f32_e32 v38, 1.0, v38
	v_add_f32_e32 v39, 1.0, v39
	v_rcp_f32_e32 v38, v38
	v_rcp_f32_e32 v39, v39
	s_nop 0
	v_pk_mul_f32 v[36:37], v[38:39], v[36:37]
	s_nop 0
	v_pk_mul_f32 v[34:35], v[34:35], v[36:37]
	s_nop 0
	v_cvt_pk_bf16_f32 v33, v34, v35
	global_store_dwordx2 v[66:67], v[32:33], off offset:32
	global_load_dwordx2 v[36:37], v[72:73], off offset:48
	s_nop 0
	global_load_dwordx4 v[32:35], v[104:105], off offset:96
	s_waitcnt vmcnt(1)
	v_lshlrev_b32_e32 v38, 16, v36
	v_and_b32_e32 v39, 0xffff0000, v36
	v_mul_f32_e32 v36, 0xbfb8aa3b, v38
	v_exp_f32_e32 v36, v36
	s_waitcnt vmcnt(0)
	v_pk_mul_f32 v[32:33], v[42:43], v[32:33]
	v_pk_mul_f32 v[42:43], v[48:49], v[64:65] op_sel_hi:[1,0]
	v_add_f32_e32 v36, 1.0, v36
	v_rcp_f32_e32 v40, v36
	v_mul_f32_e32 v36, 0xbfb8aa3b, v39
	v_exp_f32_e32 v36, v36
	s_nop 0
	v_add_f32_e32 v36, 1.0, v36
	v_rcp_f32_e32 v41, v36
	v_lshlrev_b32_e32 v36, 16, v37
	v_and_b32_e32 v37, 0xffff0000, v37
	v_pk_mul_f32 v[38:39], v[40:41], v[38:39]
	s_nop 0
	v_pk_mul_f32 v[32:33], v[32:33], v[38:39]
	v_mul_f32_e32 v38, 0xbfb8aa3b, v36
	v_mul_f32_e32 v39, 0xbfb8aa3b, v37
	v_exp_f32_e32 v38, v38
	v_exp_f32_e32 v39, v39
	v_pk_mul_f32 v[40:41], v[46:47], v[64:65] op_sel_hi:[1,0]
	v_cvt_pk_bf16_f32 v32, v32, v33
	v_add_f32_e32 v38, 1.0, v38
	v_add_f32_e32 v39, 1.0, v39
	v_rcp_f32_e32 v38, v38
	v_rcp_f32_e32 v39, v39
	v_pk_mul_f32 v[34:35], v[40:41], v[34:35]
	v_pk_mul_f32 v[36:37], v[38:39], v[36:37]
	s_nop 0
	v_pk_mul_f32 v[34:35], v[34:35], v[36:37]
	s_nop 0
	v_cvt_pk_bf16_f32 v33, v34, v35
	global_store_dwordx2 v[66:67], v[32:33], off offset:48
	global_load_dwordx2 v[36:37], v[72:73], off offset:64
	s_nop 0
	global_load_dwordx4 v[32:35], v[104:105], off offset:128
	s_waitcnt vmcnt(1)
	v_lshlrev_b32_e32 v38, 16, v36
	v_and_b32_e32 v39, 0xffff0000, v36
	v_mul_f32_e32 v36, 0xbfb8aa3b, v38
	v_exp_f32_e32 v36, v36
	s_waitcnt vmcnt(0)
	v_pk_mul_f32 v[32:33], v[42:43], v[32:33]
	v_pk_mul_f32 v[42:43], v[52:53], v[64:65] op_sel_hi:[1,0]
	v_add_f32_e32 v36, 1.0, v36
	v_rcp_f32_e32 v40, v36
	v_mul_f32_e32 v36, 0xbfb8aa3b, v39
	v_exp_f32_e32 v36, v36
	s_nop 0
	v_add_f32_e32 v36, 1.0, v36
	v_rcp_f32_e32 v41, v36
	v_lshlrev_b32_e32 v36, 16, v37
	v_and_b32_e32 v37, 0xffff0000, v37
	v_pk_mul_f32 v[38:39], v[40:41], v[38:39]
	s_nop 0
	v_pk_mul_f32 v[32:33], v[32:33], v[38:39]
	v_mul_f32_e32 v38, 0xbfb8aa3b, v36
	v_mul_f32_e32 v39, 0xbfb8aa3b, v37
	v_exp_f32_e32 v38, v38
	v_exp_f32_e32 v39, v39
	v_pk_mul_f32 v[40:41], v[50:51], v[64:65] op_sel_hi:[1,0]
	v_cvt_pk_bf16_f32 v32, v32, v33
	v_add_f32_e32 v38, 1.0, v38
	v_add_f32_e32 v39, 1.0, v39
	v_rcp_f32_e32 v38, v38
	v_rcp_f32_e32 v39, v39
	v_pk_mul_f32 v[34:35], v[40:41], v[34:35]
	v_pk_mul_f32 v[36:37], v[38:39], v[36:37]
	s_nop 0
	v_pk_mul_f32 v[34:35], v[34:35], v[36:37]
	s_nop 0
	v_cvt_pk_bf16_f32 v33, v34, v35
	global_store_dwordx2 v[66:67], v[32:33], off offset:64
	global_load_dwordx2 v[36:37], v[72:73], off offset:80
	s_nop 0
	global_load_dwordx4 v[32:35], v[104:105], off offset:160
	s_waitcnt vmcnt(1)
	v_lshlrev_b32_e32 v38, 16, v36
	v_and_b32_e32 v39, 0xffff0000, v36
	v_mul_f32_e32 v36, 0xbfb8aa3b, v38
	v_exp_f32_e32 v36, v36
	s_waitcnt vmcnt(0)
	v_pk_mul_f32 v[32:33], v[42:43], v[32:33]
	v_pk_mul_f32 v[42:43], v[56:57], v[64:65] op_sel_hi:[1,0]
	v_add_f32_e32 v36, 1.0, v36
	v_rcp_f32_e32 v40, v36
	v_mul_f32_e32 v36, 0xbfb8aa3b, v39
	v_exp_f32_e32 v36, v36
	s_nop 0
	v_add_f32_e32 v36, 1.0, v36
	v_rcp_f32_e32 v41, v36
	v_lshlrev_b32_e32 v36, 16, v37
	v_and_b32_e32 v37, 0xffff0000, v37
	v_pk_mul_f32 v[38:39], v[40:41], v[38:39]
	s_nop 0
	v_pk_mul_f32 v[32:33], v[32:33], v[38:39]
	v_mul_f32_e32 v38, 0xbfb8aa3b, v36
	v_mul_f32_e32 v39, 0xbfb8aa3b, v37
	v_exp_f32_e32 v38, v38
	v_exp_f32_e32 v39, v39
	v_pk_mul_f32 v[40:41], v[54:55], v[64:65] op_sel_hi:[1,0]
	v_cvt_pk_bf16_f32 v32, v32, v33
	v_add_f32_e32 v38, 1.0, v38
	v_add_f32_e32 v39, 1.0, v39
	v_rcp_f32_e32 v38, v38
	v_rcp_f32_e32 v39, v39
	v_pk_mul_f32 v[34:35], v[40:41], v[34:35]
	v_pk_mul_f32 v[36:37], v[38:39], v[36:37]
	s_nop 0
	v_pk_mul_f32 v[34:35], v[34:35], v[36:37]
	s_nop 0
	v_cvt_pk_bf16_f32 v33, v34, v35
	global_store_dwordx2 v[66:67], v[32:33], off offset:80
	global_load_dwordx2 v[36:37], v[72:73], off offset:96
	s_nop 0
	global_load_dwordx4 v[32:35], v[104:105], off offset:192
	s_waitcnt vmcnt(1)
	v_lshlrev_b32_e32 v38, 16, v36
	v_and_b32_e32 v39, 0xffff0000, v36
	v_mul_f32_e32 v36, 0xbfb8aa3b, v38
	v_exp_f32_e32 v36, v36
	s_waitcnt vmcnt(0)
	v_pk_mul_f32 v[32:33], v[42:43], v[32:33]
	v_pk_mul_f32 v[42:43], v[60:61], v[64:65] op_sel_hi:[1,0]
	v_add_f32_e32 v36, 1.0, v36
	v_rcp_f32_e32 v40, v36
	v_mul_f32_e32 v36, 0xbfb8aa3b, v39
	v_exp_f32_e32 v36, v36
	s_nop 0
	v_add_f32_e32 v36, 1.0, v36
	v_rcp_f32_e32 v41, v36
	v_lshlrev_b32_e32 v36, 16, v37
	v_and_b32_e32 v37, 0xffff0000, v37
	v_pk_mul_f32 v[38:39], v[40:41], v[38:39]
	s_nop 0
	v_pk_mul_f32 v[32:33], v[32:33], v[38:39]
	v_mul_f32_e32 v38, 0xbfb8aa3b, v36
	v_mul_f32_e32 v39, 0xbfb8aa3b, v37
	v_exp_f32_e32 v38, v38
	v_exp_f32_e32 v39, v39
	v_pk_mul_f32 v[40:41], v[58:59], v[64:65] op_sel_hi:[1,0]
	v_cvt_pk_bf16_f32 v32, v32, v33
	v_add_f32_e32 v38, 1.0, v38
	v_add_f32_e32 v39, 1.0, v39
	v_rcp_f32_e32 v38, v38
	v_rcp_f32_e32 v39, v39
	v_pk_mul_f32 v[34:35], v[40:41], v[34:35]
	v_pk_mul_f32 v[36:37], v[38:39], v[36:37]
	s_nop 0
	v_pk_mul_f32 v[34:35], v[34:35], v[36:37]
	s_nop 0
	v_cvt_pk_bf16_f32 v33, v34, v35
	global_store_dwordx2 v[66:67], v[32:33], off offset:96
	global_load_dwordx2 v[36:37], v[72:73], off offset:112
	s_nop 0
	global_load_dwordx4 v[32:35], v[104:105], off offset:224
	s_waitcnt vmcnt(1)
	v_lshlrev_b32_e32 v38, 16, v36
	v_and_b32_e32 v39, 0xffff0000, v36
	v_mul_f32_e32 v36, 0xbfb8aa3b, v38
	v_exp_f32_e32 v36, v36
	s_waitcnt vmcnt(0)
	v_pk_mul_f32 v[32:33], v[42:43], v[32:33]
	v_add_f32_e32 v36, 1.0, v36
	v_rcp_f32_e32 v40, v36
	v_mul_f32_e32 v36, 0xbfb8aa3b, v39
	v_exp_f32_e32 v36, v36
	s_nop 0
	v_add_f32_e32 v36, 1.0, v36
	v_rcp_f32_e32 v41, v36
	v_lshlrev_b32_e32 v36, 16, v37
	v_and_b32_e32 v37, 0xffff0000, v37
	v_pk_mul_f32 v[38:39], v[40:41], v[38:39]
	s_nop 0
	v_pk_mul_f32 v[32:33], v[32:33], v[38:39]
	v_mul_f32_e32 v38, 0xbfb8aa3b, v36
	v_mul_f32_e32 v39, 0xbfb8aa3b, v37
	v_exp_f32_e32 v38, v38
	v_exp_f32_e32 v39, v39
	v_pk_mul_f32 v[40:41], v[62:63], v[64:65] op_sel_hi:[1,0]
	v_cvt_pk_bf16_f32 v32, v32, v33
	v_add_f32_e32 v38, 1.0, v38
	v_add_f32_e32 v39, 1.0, v39
	v_rcp_f32_e32 v38, v38
	v_rcp_f32_e32 v39, v39
	v_pk_mul_f32 v[34:35], v[40:41], v[34:35]
	v_mov_b32_e32 v41, s15
	v_or_b32_e32 v40, s14, v102
	v_pk_mul_f32 v[36:37], v[38:39], v[36:37]
	s_nop 0
	v_pk_mul_f32 v[34:35], v[34:35], v[36:37]
	s_nop 0
	v_cvt_pk_bf16_f32 v33, v34, v35
	v_mul_f32_e32 v34, v17, v17
	v_fmac_f32_e32 v34, v16, v16
	v_fmac_f32_e32 v34, v18, v18
	v_fmac_f32_e32 v34, v19, v19
	v_fmac_f32_e32 v34, v20, v20
	v_fmac_f32_e32 v34, v21, v21
	v_fmac_f32_e32 v34, v22, v22
	v_fmac_f32_e32 v34, v23, v23
	v_fmac_f32_e32 v34, v24, v24
	v_fmac_f32_e32 v34, v25, v25
	v_fmac_f32_e32 v34, v26, v26
	v_fmac_f32_e32 v34, v27, v27
	v_fmac_f32_e32 v34, v28, v28
	v_fmac_f32_e32 v34, v29, v29
	v_fmac_f32_e32 v34, v30, v30
	v_fmac_f32_e32 v34, v31, v31
	v_fmac_f32_e32 v34, v0, v0
	v_fmac_f32_e32 v34, v1, v1
	v_fmac_f32_e32 v34, v2, v2
	v_fmac_f32_e32 v34, v3, v3
	v_fmac_f32_e32 v34, v4, v4
	v_fmac_f32_e32 v34, v5, v5
	v_fmac_f32_e32 v34, v6, v6
	v_fmac_f32_e32 v34, v7, v7
	v_fmac_f32_e32 v34, v8, v8
	v_fmac_f32_e32 v34, v9, v9
	v_fmac_f32_e32 v34, v10, v10
	v_fmac_f32_e32 v34, v11, v11
	v_fmac_f32_e32 v34, v12, v12
	global_store_dwordx2 v[66:67], v[32:33], off offset:112
	v_fmac_f32_e32 v34, v13, v13
	v_pk_mul_f32 v[32:33], v[14:15], v[14:15]
	s_nop 0
	v_add_f32_e32 v32, v32, v34
	v_add_f32_e32 v32, v33, v32
	v_mov_b32_e32 v33, v32
	s_nop 1
	v_permlane32_swap_b32_e32 v32, v33
	v_add_f32_e32 v32, v32, v33
	v_fmamk_f32 v32, v32, 0x3c800000, v241
	v_cmp_gt_f32_e32 vcc, s1, v32
	v_mul_f32_e32 v33, 0x4f800000, v32
	s_nop 0
	v_cndmask_b32_e32 v32, v32, v33, vcc
	v_sqrt_f32_e32 v33, v32
	s_nop 0
	v_add_u32_e32 v34, -1, v33
	v_fma_f32 v35, -v34, v33, v32
	v_cmp_ge_f32_e64 s[2:3], 0, v35
	v_add_u32_e32 v35, 1, v33
	s_nop 0
	v_cndmask_b32_e64 v34, v33, v34, s[2:3]
	v_fma_f32 v33, -v35, v33, v32
	v_cmp_lt_f32_e64 s[2:3], 0, v33
	s_nop 1
	v_cndmask_b32_e64 v33, v34, v35, s[2:3]
	v_mul_f32_e32 v34, 0x37800000, v33
	v_cndmask_b32_e32 v33, v33, v34, vcc
	v_cmp_class_f32_e32 vcc, v32, v240
	s_nop 1
	v_cndmask_b32_e32 v32, v33, v32, vcc
	v_div_scale_f32 v33, s[2:3], v32, v32, 1.0
	v_rcp_f32_e32 v34, v33
	s_nop 0
	v_fma_f32 v35, -v33, v34, 1.0
	v_fmac_f32_e32 v34, v35, v34
	v_div_scale_f32 v35, vcc, 1.0, v32, 1.0
	v_mul_f32_e32 v36, v35, v34
	v_fma_f32 v37, -v33, v36, v35
	v_fmac_f32_e32 v36, v37, v34
	v_fma_f32 v33, -v33, v36, v35
	v_div_fmas_f32 v33, v33, v34, v36
	v_lshlrev_b64 v[34:35], 9, v[40:41]
	v_lshl_add_u64 v[34:35], v[106:107], 0, v[34:35]
	global_load_dwordx2 v[42:43], v[34:35], off
	global_load_dwordx4 v[36:39], v[104:105], off
	v_div_fixup_f32 v32, v33, v32, 1.0
	s_waitcnt vmcnt(1)
	v_lshlrev_b32_e32 v44, 16, v42
	v_mul_f32_e32 v33, 0xbfb8aa3b, v44
	v_exp_f32_e32 v33, v33
	v_and_b32_e32 v45, 0xffff0000, v42
	v_add_f32_e32 v33, 1.0, v33
	v_rcp_f32_e32 v46, v33
	v_pk_mul_f32 v[16:17], v[16:17], v[32:33] op_sel_hi:[1,0]
	v_mul_f32_e32 v33, 0xbfb8aa3b, v45
	v_exp_f32_e32 v33, v33
	s_waitcnt vmcnt(0)
	v_pk_mul_f32 v[16:17], v[36:37], v[16:17]
	v_add_f32_e32 v33, 1.0, v33
	v_rcp_f32_e32 v47, v33
	s_nop 0
	v_pk_mul_f32 v[36:37], v[46:47], v[44:45]
	s_nop 0
	v_pk_mul_f32 v[16:17], v[16:17], v[36:37]
	v_lshlrev_b32_e32 v36, 16, v43
	v_mul_f32_e32 v33, 0xbfb8aa3b, v36
	v_exp_f32_e32 v33, v33
	v_and_b32_e32 v37, 0xffff0000, v43
	v_add_f32_e32 v33, 1.0, v33
	v_rcp_f32_e32 v42, v33
	v_pk_mul_f32 v[18:19], v[18:19], v[32:33] op_sel_hi:[1,0]
	v_mul_f32_e32 v33, 0xbfb8aa3b, v37
	v_exp_f32_e32 v33, v33
	v_pk_mul_f32 v[18:19], v[38:39], v[18:19]
	v_add_f32_e32 v33, 1.0, v33
	v_rcp_f32_e32 v43, v33
	v_pk_mul_f32 v[20:21], v[20:21], v[32:33] op_sel_hi:[1,0]
	v_pk_mul_f32 v[36:37], v[42:43], v[36:37]
	s_nop 0
	v_pk_mul_f32 v[36:37], v[18:19], v[36:37]
	v_cvt_pk_bf16_f32 v18, v16, v17
	v_mad_u64_u32 v[16:17], s[2:3], v40, s83, v[108:109]
	v_cvt_pk_bf16_f32 v19, v36, v37
	v_mad_i32_i24 v17, s15, v227, v17
	global_store_dwordx2 v[16:17], v[18:19], off
	global_load_dwordx2 v[18:19], v[34:35], off offset:16
	s_nop 0
	global_load_dwordx4 v[36:39], v[104:105], off offset:32
	s_waitcnt vmcnt(1)
	v_lshlrev_b32_e32 v40, 16, v18
	v_and_b32_e32 v41, 0xffff0000, v18
	v_mul_f32_e32 v18, 0xbfb8aa3b, v40
	v_exp_f32_e32 v18, v18
	s_waitcnt vmcnt(0)
	v_pk_mul_f32 v[20:21], v[36:37], v[20:21]
	v_add_f32_e32 v18, 1.0, v18
	v_rcp_f32_e32 v42, v18
	v_mul_f32_e32 v18, 0xbfb8aa3b, v41
	v_exp_f32_e32 v18, v18
	s_nop 0
	v_add_f32_e32 v18, 1.0, v18
	v_rcp_f32_e32 v43, v18
	v_lshlrev_b32_e32 v18, 16, v19
	v_mul_f32_e32 v33, 0xbfb8aa3b, v18
	v_exp_f32_e32 v33, v33
	v_pk_mul_f32 v[36:37], v[42:43], v[40:41]
	v_and_b32_e32 v19, 0xffff0000, v19
	v_pk_mul_f32 v[20:21], v[20:21], v[36:37]
	v_add_f32_e32 v33, 1.0, v33
	v_rcp_f32_e32 v36, v33
	v_pk_mul_f32 v[22:23], v[22:23], v[32:33] op_sel_hi:[1,0]
	v_mul_f32_e32 v33, 0xbfb8aa3b, v19
	v_exp_f32_e32 v33, v33
	v_pk_mul_f32 v[22:23], v[38:39], v[22:23]
	v_cvt_pk_bf16_f32 v20, v20, v21
	v_add_f32_e32 v33, 1.0, v33
	v_rcp_f32_e32 v37, v33
	v_pk_mul_f32 v[24:25], v[24:25], v[32:33] op_sel_hi:[1,0]
	v_pk_mul_f32 v[26:27], v[26:27], v[32:33] op_sel_hi:[1,0]
	v_pk_mul_f32 v[28:29], v[28:29], v[32:33] op_sel_hi:[1,0]
	v_pk_mul_f32 v[18:19], v[36:37], v[18:19]
	v_pk_mul_f32 v[0:1], v[0:1], v[32:33] op_sel_hi:[1,0]
	v_pk_mul_f32 v[18:19], v[22:23], v[18:19]
	v_pk_mul_f32 v[2:3], v[2:3], v[32:33] op_sel_hi:[1,0]
	v_cvt_pk_bf16_f32 v21, v18, v19
	global_store_dwordx2 v[16:17], v[20:21], off offset:16
	global_load_dwordx2 v[22:23], v[34:35], off offset:32
	s_nop 0
	global_load_dwordx4 v[18:21], v[104:105], off offset:64
	v_pk_mul_f32 v[4:5], v[4:5], v[32:33] op_sel_hi:[1,0]
	v_pk_mul_f32 v[6:7], v[6:7], v[32:33] op_sel_hi:[1,0]
	v_pk_mul_f32 v[8:9], v[8:9], v[32:33] op_sel_hi:[1,0]
	s_waitcnt vmcnt(1)
	v_lshlrev_b32_e32 v36, 16, v22
	v_and_b32_e32 v37, 0xffff0000, v22
	v_mul_f32_e32 v22, 0xbfb8aa3b, v36
	v_exp_f32_e32 v22, v22
	s_waitcnt vmcnt(0)
	v_pk_mul_f32 v[18:19], v[24:25], v[18:19]
	v_pk_mul_f32 v[20:21], v[26:27], v[20:21]
	v_add_f32_e32 v22, 1.0, v22
	v_rcp_f32_e32 v38, v22
	v_mul_f32_e32 v22, 0xbfb8aa3b, v37
	v_exp_f32_e32 v22, v22
	s_nop 0
	v_add_f32_e32 v22, 1.0, v22
	v_rcp_f32_e32 v39, v22
	v_lshlrev_b32_e32 v22, 16, v23
	v_and_b32_e32 v23, 0xffff0000, v23
	v_pk_mul_f32 v[24:25], v[38:39], v[36:37]
	s_nop 0
	v_pk_mul_f32 v[18:19], v[18:19], v[24:25]
	v_mul_f32_e32 v24, 0xbfb8aa3b, v22
	v_mul_f32_e32 v25, 0xbfb8aa3b, v23
	v_exp_f32_e32 v24, v24
	v_exp_f32_e32 v25, v25
	v_cvt_pk_bf16_f32 v18, v18, v19
	v_add_f32_e32 v24, 1.0, v24
	v_add_f32_e32 v25, 1.0, v25
	v_rcp_f32_e32 v24, v24
	v_rcp_f32_e32 v25, v25
	s_nop 0
	v_pk_mul_f32 v[22:23], v[24:25], v[22:23]
	s_nop 0
	v_pk_mul_f32 v[20:21], v[20:21], v[22:23]
	s_nop 0
	v_cvt_pk_bf16_f32 v19, v20, v21
	global_store_dwordx2 v[16:17], v[18:19], off offset:32
	global_load_dwordx2 v[18:19], v[34:35], off offset:48
	s_nop 0
	global_load_dwordx4 v[20:23], v[104:105], off offset:96
	s_waitcnt vmcnt(1)
	v_lshlrev_b32_e32 v24, 16, v18
	v_and_b32_e32 v25, 0xffff0000, v18
	v_mul_f32_e32 v18, 0xbfb8aa3b, v24
	v_exp_f32_e32 v18, v18
	s_waitcnt vmcnt(0)
	v_pk_mul_f32 v[20:21], v[28:29], v[20:21]
	v_add_f32_e32 v18, 1.0, v18
	v_rcp_f32_e32 v26, v18
	v_mul_f32_e32 v18, 0xbfb8aa3b, v25
	v_exp_f32_e32 v18, v18
	s_nop 0
	v_add_f32_e32 v18, 1.0, v18
	v_rcp_f32_e32 v27, v18
	v_lshlrev_b32_e32 v18, 16, v19
	v_and_b32_e32 v19, 0xffff0000, v19
	v_pk_mul_f32 v[24:25], v[26:27], v[24:25]
	s_nop 0
	v_pk_mul_f32 v[20:21], v[20:21], v[24:25]
	v_mul_f32_e32 v24, 0xbfb8aa3b, v18
	v_mul_f32_e32 v25, 0xbfb8aa3b, v19
	v_exp_f32_e32 v24, v24
	v_exp_f32_e32 v25, v25
	v_pk_mul_f32 v[26:27], v[30:31], v[32:33] op_sel_hi:[1,0]
	v_cvt_pk_bf16_f32 v20, v20, v21
	v_add_f32_e32 v24, 1.0, v24
	v_add_f32_e32 v25, 1.0, v25
	v_rcp_f32_e32 v24, v24
	v_rcp_f32_e32 v25, v25
	v_pk_mul_f32 v[22:23], v[26:27], v[22:23]
	v_pk_mul_f32 v[18:19], v[24:25], v[18:19]
	s_nop 0
	v_pk_mul_f32 v[18:19], v[22:23], v[18:19]
	s_nop 0
	v_cvt_pk_bf16_f32 v21, v18, v19
	global_store_dwordx2 v[16:17], v[20:21], off offset:48
	global_load_dwordx2 v[22:23], v[34:35], off offset:64
	s_nop 0
	global_load_dwordx4 v[18:21], v[104:105], off offset:128
	s_waitcnt vmcnt(1)
	v_lshlrev_b32_e32 v24, 16, v22
	v_and_b32_e32 v25, 0xffff0000, v22
	v_mul_f32_e32 v22, 0xbfb8aa3b, v24
	s_waitcnt vmcnt(0)
	v_pk_mul_f32 v[0:1], v[0:1], v[18:19]
	v_mul_f32_e32 v18, 0xbfb8aa3b, v25
	v_exp_f32_e32 v22, v22
	v_exp_f32_e32 v18, v18
	v_pk_mul_f32 v[2:3], v[2:3], v[20:21]
	v_add_f32_e32 v22, 1.0, v22
	v_add_f32_e32 v18, 1.0, v18
	v_rcp_f32_e32 v26, v22
	v_rcp_f32_e32 v27, v18
	s_nop 0
	v_pk_mul_f32 v[18:19], v[26:27], v[24:25]
	s_nop 0
	v_pk_mul_f32 v[0:1], v[0:1], v[18:19]
	v_lshlrev_b32_e32 v18, 16, v23
	v_and_b32_e32 v19, 0xffff0000, v23
	v_mul_f32_e32 v22, 0xbfb8aa3b, v18
	v_mul_f32_e32 v20, 0xbfb8aa3b, v19
	v_exp_f32_e32 v22, v22
	v_exp_f32_e32 v20, v20
	v_cvt_pk_bf16_f32 v0, v0, v1
	v_add_f32_e32 v22, 1.0, v22
	v_add_f32_e32 v20, 1.0, v20
	v_rcp_f32_e32 v22, v22
	v_rcp_f32_e32 v23, v20
	s_nop 0
	v_pk_mul_f32 v[18:19], v[22:23], v[18:19]
	s_nop 0
	v_pk_mul_f32 v[2:3], v[2:3], v[18:19]
	s_nop 0
	v_cvt_pk_bf16_f32 v1, v2, v3
	global_store_dwordx2 v[16:17], v[0:1], off offset:64
	global_load_dwordx2 v[18:19], v[34:35], off offset:80
	s_nop 0
	global_load_dwordx4 v[0:3], v[104:105], off offset:160
	s_waitcnt vmcnt(1)
	v_lshlrev_b32_e32 v20, 16, v18
	v_and_b32_e32 v21, 0xffff0000, v18
	v_mul_f32_e32 v18, 0xbfb8aa3b, v20
	s_waitcnt vmcnt(0)
	v_pk_mul_f32 v[0:1], v[4:5], v[0:1]
	v_mul_f32_e32 v4, 0xbfb8aa3b, v21
	v_exp_f32_e32 v18, v18
	v_exp_f32_e32 v4, v4
	v_pk_mul_f32 v[2:3], v[6:7], v[2:3]
	v_add_f32_e32 v18, 1.0, v18
	v_add_f32_e32 v4, 1.0, v4
	v_rcp_f32_e32 v22, v18
	v_rcp_f32_e32 v23, v4
	s_nop 0
	v_pk_mul_f32 v[4:5], v[22:23], v[20:21]
	s_nop 0
	v_pk_mul_f32 v[0:1], v[0:1], v[4:5]
	v_lshlrev_b32_e32 v4, 16, v19
	v_and_b32_e32 v5, 0xffff0000, v19
	v_mul_f32_e32 v18, 0xbfb8aa3b, v4
	v_mul_f32_e32 v6, 0xbfb8aa3b, v5
	v_exp_f32_e32 v18, v18
	v_exp_f32_e32 v6, v6
	v_cvt_pk_bf16_f32 v0, v0, v1
	v_add_f32_e32 v18, 1.0, v18
	v_add_f32_e32 v6, 1.0, v6
	v_rcp_f32_e32 v18, v18
	v_rcp_f32_e32 v19, v6
	s_nop 0
	v_pk_mul_f32 v[4:5], v[18:19], v[4:5]
	s_nop 0
	v_pk_mul_f32 v[2:3], v[2:3], v[4:5]
	s_nop 0
	v_cvt_pk_bf16_f32 v1, v2, v3
	global_store_dwordx2 v[16:17], v[0:1], off offset:80
	global_load_dwordx2 v[4:5], v[34:35], off offset:96
	s_nop 0
	global_load_dwordx4 v[0:3], v[104:105], off offset:192
	s_waitcnt vmcnt(1)
	v_lshlrev_b32_e32 v6, 16, v4
	v_and_b32_e32 v7, 0xffff0000, v4
	v_mul_f32_e32 v4, 0xbfb8aa3b, v6
	v_exp_f32_e32 v4, v4
	s_waitcnt vmcnt(0)
	v_pk_mul_f32 v[0:1], v[8:9], v[0:1]
	v_pk_mul_f32 v[8:9], v[10:11], v[32:33] op_sel_hi:[1,0]
	v_pk_mul_f32 v[10:11], v[12:13], v[32:33] op_sel_hi:[1,0]
	v_add_f32_e32 v4, 1.0, v4
	v_rcp_f32_e32 v18, v4
	v_mul_f32_e32 v4, 0xbfb8aa3b, v7
	v_exp_f32_e32 v4, v4
	v_pk_mul_f32 v[2:3], v[8:9], v[2:3]
	v_add_f32_e32 v4, 1.0, v4
	v_rcp_f32_e32 v19, v4
	v_lshlrev_b32_e32 v4, 16, v5
	v_and_b32_e32 v5, 0xffff0000, v5
	v_pk_mul_f32 v[6:7], v[18:19], v[6:7]
	s_nop 0
	v_pk_mul_f32 v[0:1], v[0:1], v[6:7]
	v_mul_f32_e32 v6, 0xbfb8aa3b, v4
	v_mul_f32_e32 v7, 0xbfb8aa3b, v5
	v_exp_f32_e32 v6, v6
	v_exp_f32_e32 v7, v7
	v_cvt_pk_bf16_f32 v0, v0, v1
	v_add_f32_e32 v6, 1.0, v6
	v_add_f32_e32 v7, 1.0, v7
	v_rcp_f32_e32 v6, v6
	v_rcp_f32_e32 v7, v7
	s_nop 0
	v_pk_mul_f32 v[4:5], v[6:7], v[4:5]
	s_nop 0
	v_pk_mul_f32 v[2:3], v[2:3], v[4:5]
	s_nop 0
	v_cvt_pk_bf16_f32 v1, v2, v3
	global_store_dwordx2 v[16:17], v[0:1], off offset:96
	global_load_dwordx2 v[0:1], v[34:35], off offset:112
	s_nop 0
	global_load_dwordx4 v[2:5], v[104:105], off offset:224
	s_waitcnt vmcnt(1)
	v_lshlrev_b32_e32 v6, 16, v0
	v_and_b32_e32 v7, 0xffff0000, v0
	v_mul_f32_e32 v0, 0xbfb8aa3b, v6
	v_exp_f32_e32 v0, v0
	s_waitcnt vmcnt(0)
	v_pk_mul_f32 v[2:3], v[10:11], v[2:3]
	v_add_f32_e32 v0, 1.0, v0
	v_rcp_f32_e32 v8, v0
	v_mul_f32_e32 v0, 0xbfb8aa3b, v7
	v_exp_f32_e32 v0, v0
	s_nop 0
	v_add_f32_e32 v0, 1.0, v0
	v_rcp_f32_e32 v9, v0
	v_lshlrev_b32_e32 v0, 16, v1
	v_and_b32_e32 v1, 0xffff0000, v1
	v_pk_mul_f32 v[6:7], v[8:9], v[6:7]
	s_nop 0
	v_pk_mul_f32 v[2:3], v[2:3], v[6:7]
	v_mul_f32_e32 v6, 0xbfb8aa3b, v0
	v_mul_f32_e32 v7, 0xbfb8aa3b, v1
	v_exp_f32_e32 v6, v6
	v_exp_f32_e32 v7, v7
	v_pk_mul_f32 v[8:9], v[14:15], v[32:33] op_sel_hi:[1,0]
	v_cvt_pk_bf16_f32 v2, v2, v3
	v_add_f32_e32 v6, 1.0, v6
	v_add_f32_e32 v7, 1.0, v7
	v_rcp_f32_e32 v6, v6
	v_rcp_f32_e32 v7, v7
	v_pk_mul_f32 v[4:5], v[8:9], v[4:5]
	v_pk_mul_f32 v[0:1], v[6:7], v[0:1]
	s_nop 0
	v_pk_mul_f32 v[0:1], v[4:5], v[0:1]
	s_nop 0
	v_cvt_pk_bf16_f32 v3, v0, v1
	global_store_dwordx2 v[16:17], v[2:3], off offset:112
	s_waitcnt lgkmcnt(0)
	s_cbranch_scc0 .LBB0_768
	v_readlane_b32 s75, v254, 28
	s_mov_b32 s76, s18
	v_readlane_b32 s79, v254, 33
	s_mov_b64 s[46:47], s[20:21]
	v_readlane_b32 s44, v254, 38
